# v43 + MoE weight-conversion f32 loads (read once) marked nt
# baseline (speedup 1.0000x reference)
.LBB0_361:
	v_mov_b32_e32 v6, v172
	s_cmpk_gt_u32 s20, 0x7fff
	s_mov_b64 s[0:1], -1
	s_cbranch_scc0 .LBB0_363
	s_add_i32 s0, s20, 0xffff8000
	s_lshr_b32 s8, s0, 9
	s_lshl_b64 s[0:1], s[8:9], 20
	s_lshl_b64 s[74:75], s[8:9], 22
	s_add_u32 s76, s14, s74
	s_addc_u32 s75, s15, s75
	s_add_u32 s0, s26, s0
	s_addc_u32 s1, s27, s1
	s_add_i32 s8, s21, s23
	s_and_b32 s8, s8, 0x3c0
	s_and_b32 s74, s22, 0x3e0
	v_ashrrev_i32_e32 v7, 5, v6
	s_lshl_b32 s77, s74, 2
	v_add_u32_e32 v4, s8, v7
	v_and_b32_e32 v24, 31, v6
	s_add_u32 s76, s76, s77
	v_add_u32_e32 v10, 2, v4
	v_add_u32_e32 v12, 4, v4
	v_add_u32_e32 v14, 6, v4
	v_add_u32_e32 v20, 12, v4
	s_addc_u32 s77, s75, 0
	v_lshlrev_b32_e32 v0, 2, v24
	v_ashrrev_i32_e32 v5, 31, v4
	v_ashrrev_i32_e32 v11, 31, v10
	v_ashrrev_i32_e32 v13, 31, v12
	v_ashrrev_i32_e32 v15, 31, v14
	v_add_u32_e32 v16, 8, v4
	v_add_u32_e32 v18, 10, v4
	v_ashrrev_i32_e32 v21, 31, v20
	v_add_u32_e32 v22, 14, v4
	v_lshl_add_u64 v[2:3], s[76:77], 0, v[0:1]
	v_lshlrev_b64 v[8:9], 12, v[4:5]
	v_lshlrev_b64 v[10:11], 12, v[10:11]
	v_lshlrev_b64 v[12:13], 12, v[12:13]
	v_lshlrev_b64 v[14:15], 12, v[14:15]
	v_ashrrev_i32_e32 v17, 31, v16
	v_ashrrev_i32_e32 v19, 31, v18
	v_lshlrev_b64 v[20:21], 12, v[20:21]
	v_ashrrev_i32_e32 v23, 31, v22
	v_lshl_add_u64 v[8:9], v[2:3], 0, v[8:9]
	v_lshl_add_u64 v[10:11], v[2:3], 0, v[10:11]
	v_lshl_add_u64 v[12:13], v[2:3], 0, v[12:13]
	v_lshl_add_u64 v[14:15], v[2:3], 0, v[14:15]
	v_lshlrev_b64 v[16:17], 12, v[16:17]
	v_lshlrev_b64 v[18:19], 12, v[18:19]
	v_lshl_add_u64 v[20:21], v[2:3], 0, v[20:21]
	v_lshlrev_b64 v[22:23], 12, v[22:23]
	v_lshl_add_u64 v[16:17], v[2:3], 0, v[16:17]
	v_lshl_add_u64 v[18:19], v[2:3], 0, v[18:19]
	v_lshl_add_u64 v[22:23], v[2:3], 0, v[22:23]
	global_load_dword v25, v[8:9], off nt
	global_load_dword v26, v[10:11], off nt
	global_load_dword v27, v[12:13], off nt
	global_load_dword v28, v[14:15], off nt
	global_load_dword v29, v[16:17], off nt
	global_load_dword v30, v[18:19], off nt
	global_load_dword v31, v[20:21], off nt
	global_load_dword v32, v[22:23], off nt
	v_add_u32_e32 v8, 16, v4
	v_add_u32_e32 v10, 18, v4
	v_add_u32_e32 v12, 20, v4
	v_add_u32_e32 v14, 22, v4
	v_add_u32_e32 v20, 28, v4
	v_ashrrev_i32_e32 v9, 31, v8
	v_ashrrev_i32_e32 v11, 31, v10
	v_ashrrev_i32_e32 v13, 31, v12
	v_ashrrev_i32_e32 v15, 31, v14
	v_add_u32_e32 v16, 24, v4
	v_add_u32_e32 v18, 26, v4
	v_ashrrev_i32_e32 v21, 31, v20
	v_add_u32_e32 v22, 30, v4
	v_lshlrev_b64 v[8:9], 12, v[8:9]
	v_lshlrev_b64 v[10:11], 12, v[10:11]
	v_lshlrev_b64 v[12:13], 12, v[12:13]
	v_lshlrev_b64 v[14:15], 12, v[14:15]
	v_ashrrev_i32_e32 v17, 31, v16
	v_ashrrev_i32_e32 v19, 31, v18
	v_lshlrev_b64 v[20:21], 12, v[20:21]
	v_ashrrev_i32_e32 v23, 31, v22
	v_lshl_add_u64 v[8:9], v[2:3], 0, v[8:9]
	v_lshl_add_u64 v[10:11], v[2:3], 0, v[10:11]
	v_lshl_add_u64 v[12:13], v[2:3], 0, v[12:13]
	v_lshl_add_u64 v[14:15], v[2:3], 0, v[14:15]
	v_lshlrev_b64 v[16:17], 12, v[16:17]
	v_lshlrev_b64 v[18:19], 12, v[18:19]
	v_lshl_add_u64 v[20:21], v[2:3], 0, v[20:21]
	v_lshlrev_b64 v[22:23], 12, v[22:23]
	v_lshl_add_u64 v[16:17], v[2:3], 0, v[16:17]
	v_lshl_add_u64 v[18:19], v[2:3], 0, v[18:19]
	v_lshl_add_u64 v[22:23], v[2:3], 0, v[22:23]
	global_load_dword v33, v[8:9], off nt
	global_load_dword v34, v[10:11], off nt
	global_load_dword v35, v[12:13], off nt
	global_load_dword v36, v[14:15], off nt
	global_load_dword v37, v[16:17], off nt
	global_load_dword v38, v[18:19], off nt
	global_load_dword v39, v[20:21], off nt
	global_load_dword v40, v[22:23], off nt
	v_add_u32_e32 v8, 32, v4
	v_add_u32_e32 v10, 34, v4
	v_add_u32_e32 v12, 36, v4
	v_add_u32_e32 v14, 38, v4
	v_add_u32_e32 v20, 44, v4
	v_ashrrev_i32_e32 v9, 31, v8
	v_ashrrev_i32_e32 v11, 31, v10
	v_ashrrev_i32_e32 v13, 31, v12
	v_ashrrev_i32_e32 v15, 31, v14
	v_add_u32_e32 v16, 40, v4
	v_add_u32_e32 v18, 42, v4
	v_ashrrev_i32_e32 v21, 31, v20
	v_add_u32_e32 v22, 46, v4
	v_lshlrev_b64 v[8:9], 12, v[8:9]
	v_lshlrev_b64 v[10:11], 12, v[10:11]
	v_lshlrev_b64 v[12:13], 12, v[12:13]
	v_lshlrev_b64 v[14:15], 12, v[14:15]
	v_ashrrev_i32_e32 v17, 31, v16
	v_ashrrev_i32_e32 v19, 31, v18
	v_lshlrev_b64 v[20:21], 12, v[20:21]
	v_ashrrev_i32_e32 v23, 31, v22
	v_lshl_add_u64 v[8:9], v[2:3], 0, v[8:9]
	v_lshl_add_u64 v[10:11], v[2:3], 0, v[10:11]
	v_lshl_add_u64 v[12:13], v[2:3], 0, v[12:13]
	v_lshl_add_u64 v[14:15], v[2:3], 0, v[14:15]
	v_lshlrev_b64 v[16:17], 12, v[16:17]
	v_lshlrev_b64 v[18:19], 12, v[18:19]
	v_lshl_add_u64 v[20:21], v[2:3], 0, v[20:21]
	v_lshlrev_b64 v[22:23], 12, v[22:23]
	v_lshl_add_u64 v[16:17], v[2:3], 0, v[16:17]
	v_lshl_add_u64 v[18:19], v[2:3], 0, v[18:19]
	v_lshl_add_u64 v[22:23], v[2:3], 0, v[22:23]
	global_load_dword v41, v[8:9], off nt
	global_load_dword v42, v[10:11], off nt
	global_load_dword v43, v[12:13], off nt
	global_load_dword v44, v[14:15], off nt
	global_load_dword v45, v[16:17], off nt
	global_load_dword v46, v[18:19], off nt
	s_nop 0
	global_load_dword v20, v[20:21], off nt
	s_nop 0
	global_load_dword v21, v[22:23], off nt
	v_add_u32_e32 v8, 48, v4
	v_add_u32_e32 v10, 50, v4
	v_add_u32_e32 v12, 52, v4
	v_add_u32_e32 v14, 54, v4
	v_ashrrev_i32_e32 v9, 31, v8
	v_ashrrev_i32_e32 v11, 31, v10
	v_ashrrev_i32_e32 v13, 31, v12
	v_ashrrev_i32_e32 v15, 31, v14
	v_add_u32_e32 v16, 56, v4
	v_add_u32_e32 v18, 58, v4
	v_lshlrev_b64 v[8:9], 12, v[8:9]
	v_lshlrev_b64 v[10:11], 12, v[10:11]
	v_lshlrev_b64 v[12:13], 12, v[12:13]
	v_lshlrev_b64 v[14:15], 12, v[14:15]
	v_ashrrev_i32_e32 v17, 31, v16
	v_ashrrev_i32_e32 v19, 31, v18
	v_lshl_add_u64 v[8:9], v[2:3], 0, v[8:9]
	v_lshl_add_u64 v[10:11], v[2:3], 0, v[10:11]
	v_lshl_add_u64 v[12:13], v[2:3], 0, v[12:13]
	v_lshl_add_u64 v[14:15], v[2:3], 0, v[14:15]
	v_lshlrev_b64 v[16:17], 12, v[16:17]
	v_lshlrev_b64 v[18:19], 12, v[18:19]
	v_lshl_add_u64 v[16:17], v[2:3], 0, v[16:17]
	v_lshl_add_u64 v[18:19], v[2:3], 0, v[18:19]
	global_load_dword v22, v[8:9], off nt
	s_nop 0
	global_load_dword v10, v[10:11], off nt
	s_nop 0
	global_load_dword v11, v[12:13], off nt
	s_nop 0
	global_load_dword v12, v[14:15], off nt
	global_load_dword v13, v[16:17], off nt
	s_nop 0
	global_load_dword v14, v[18:19], off nt
	v_add_u32_e32 v8, 60, v4
	v_ashrrev_i32_e32 v9, 31, v8
	v_add_u32_e32 v4, 62, v4
	v_lshlrev_b64 v[8:9], 12, v[8:9]
	v_ashrrev_i32_e32 v5, 31, v4
	v_lshl_add_u64 v[8:9], v[2:3], 0, v[8:9]
	v_lshlrev_b64 v[4:5], 12, v[4:5]
	v_lshl_add_u64 v[2:3], v[2:3], 0, v[4:5]
	global_load_dword v4, v[8:9], off nt
	global_load_dword v5, v[2:3], off nt
	v_add_u32_e32 v0, s24, v0
	v_mad_u64_u32 v[2:3], s[76:77], v7, s72, v[0:1]
	s_waitcnt vmcnt(0)
	v_mul_f32_e32 v8, 0x42800000, v25
	v_mul_f32_e32 v3, 0x42800000, v26
	ds_write2_b32 v2, v8, v3 offset1:66
	v_mul_f32_e32 v3, 0x42800000, v27
	v_mul_f32_e32 v7, 0x42800000, v28
	ds_write2_b32 v2, v3, v7 offset0:132 offset1:198
	v_mul_f32_e32 v3, 0x42800000, v29
	v_mul_f32_e32 v7, 0x42800000, v30
	v_add_u32_e32 v8, 0x400, v2
	ds_write2_b32 v8, v3, v7 offset0:8 offset1:74
	v_mul_f32_e32 v3, 0x42800000, v31
	v_mul_f32_e32 v7, 0x42800000, v32
	ds_write2_b32 v8, v3, v7 offset0:140 offset1:206
	v_mul_f32_e32 v3, 0x42800000, v33
	v_mul_f32_e32 v7, 0x42800000, v34
	v_add_u32_e32 v8, 0x800, v2
	ds_write2_b32 v8, v3, v7 offset0:16 offset1:82
	v_mul_f32_e32 v3, 0x42800000, v35
	v_mul_f32_e32 v7, 0x42800000, v36
	ds_write2_b32 v8, v3, v7 offset0:148 offset1:214
	v_mul_f32_e32 v3, 0x42800000, v37
	v_mul_f32_e32 v7, 0x42800000, v38
	v_add_u32_e32 v8, 0xc00, v2
	ds_write2_b32 v8, v3, v7 offset0:24 offset1:90
	v_mul_f32_e32 v3, 0x42800000, v39
	v_mul_f32_e32 v7, 0x42800000, v40
	ds_write2_b32 v8, v3, v7 offset0:156 offset1:222
	v_add_u32_e32 v8, 0x1000, v2
	v_mul_f32_e32 v3, 0x42800000, v41
	v_mul_f32_e32 v7, 0x42800000, v42
	ds_write2_b32 v8, v3, v7 offset0:32 offset1:98
	v_mul_f32_e32 v3, 0x42800000, v43
	v_mul_f32_e32 v7, 0x42800000, v44
	ds_write2_b32 v8, v3, v7 offset0:164 offset1:230
	v_mul_f32_e32 v3, 0x42800000, v45
	v_mul_f32_e32 v7, 0x42800000, v46
	v_add_u32_e32 v8, 0x1400, v2
	ds_write2_b32 v8, v3, v7 offset0:40 offset1:106
	v_mul_f32_e32 v3, 0x42800000, v20
	v_mul_f32_e32 v7, 0x42800000, v21
	ds_write2_b32 v8, v3, v7 offset0:172 offset1:238
	v_add_u32_e32 v8, 0x1800, v2
	v_add_u32_e32 v2, 0x1c00, v2
	v_mul_f32_e32 v3, 0x42800000, v22
	v_mul_f32_e32 v7, 0x42800000, v10
	ds_write2_b32 v8, v3, v7 offset0:48 offset1:114
	v_mul_f32_e32 v3, 0x42800000, v11
	v_mul_f32_e32 v7, 0x42800000, v12
	ds_write2_b32 v8, v3, v7 offset0:180 offset1:246
	v_mul_f32_e32 v3, 0x42800000, v13
	v_mul_f32_e32 v7, 0x42800000, v14
	ds_write2_b32 v2, v3, v7 offset0:56 offset1:122
	v_and_b32_e32 v12, 0xffffffe0, v6
	v_mad_u64_u32 v[10:11], s[76:77], v12, s72, v[0:1]
	v_mul_f32_e32 v3, 0x42800000, v4
	v_mul_f32_e32 v4, 0x42800000, v5
	ds_write2_b32 v2, v3, v4 offset0:188 offset1:254
	s_waitcnt lgkmcnt(0)
	ds_read2_b32 v[2:3], v10 offset1:33
	ds_read2_b32 v[4:5], v10 offset0:66 offset1:99
	ds_read2_b32 v[8:9], v10 offset0:132 offset1:165
	s_waitcnt lgkmcnt(2)
	v_med3_f32 v0, v2, s73, v188
	v_med3_f32 v3, v3, s73, v188
	v_mov_b32_e32 v2, v1
	v_cvt_pk_fp8_f32 v2, v0, v3
	s_waitcnt lgkmcnt(1)
	v_med3_f32 v0, v4, s73, v188
	v_med3_f32 v3, v5, s73, v188
	s_waitcnt lgkmcnt(0)
	v_med3_f32 v7, v9, s73, v188
	v_cvt_pk_fp8_f32 v2, v0, v3 op_sel:[0,0,1]
	v_med3_f32 v0, v8, s73, v188
	v_mov_b32_e32 v3, v1
	ds_read2_b32 v[4:5], v10 offset0:198 offset1:231
	v_cvt_pk_fp8_f32 v3, v0, v7
	v_add_u32_e32 v0, 0x400, v10
	ds_read2_b32 v[8:9], v0 offset0:8 offset1:41
	ds_read2_b32 v[14:15], v0 offset0:74 offset1:107
	s_waitcnt lgkmcnt(2)
	v_med3_f32 v4, v4, s73, v188
	v_med3_f32 v5, v5, s73, v188
	v_cvt_pk_fp8_f32 v3, v4, v5 op_sel:[0,0,1]
	s_waitcnt lgkmcnt(1)
	v_med3_f32 v5, v8, s73, v188
	v_med3_f32 v7, v9, s73, v188
	v_mov_b32_e32 v4, v1
	ds_read2_b32 v[8:9], v0 offset0:140 offset1:173
	v_cvt_pk_fp8_f32 v4, v5, v7
	s_waitcnt lgkmcnt(1)
	v_med3_f32 v5, v14, s73, v188
	v_med3_f32 v7, v15, s73, v188
	ds_read2_b32 v[14:15], v0 offset0:206 offset1:239
	v_cvt_pk_fp8_f32 v4, v5, v7 op_sel:[0,0,1]
	s_waitcnt lgkmcnt(1)
	v_med3_f32 v0, v8, s73, v188
	v_med3_f32 v7, v9, s73, v188
	v_mov_b32_e32 v5, v1
	v_cvt_pk_fp8_f32 v5, v0, v7
	v_add_u32_e32 v0, 0x800, v10
	ds_read2_b32 v[8:9], v0 offset0:16 offset1:49
	s_waitcnt lgkmcnt(1)
	v_med3_f32 v7, v14, s73, v188
	v_med3_f32 v11, v15, s73, v188
	ds_read2_b32 v[14:15], v0 offset0:82 offset1:115
	v_cvt_pk_fp8_f32 v5, v7, v11 op_sel:[0,0,1]
	s_waitcnt lgkmcnt(1)
	v_med3_f32 v7, v8, s73, v188
	v_med3_f32 v9, v9, s73, v188
	v_mov_b32_e32 v8, v1
	ds_read2_b32 v[16:17], v0 offset0:148 offset1:181
	v_cvt_pk_fp8_f32 v8, v7, v9
	s_waitcnt lgkmcnt(1)
	v_med3_f32 v7, v14, s73, v188
	v_med3_f32 v9, v15, s73, v188
	ds_read2_b32 v[14:15], v0 offset0:214 offset1:247
	v_cvt_pk_fp8_f32 v8, v7, v9 op_sel:[0,0,1]
	s_waitcnt lgkmcnt(1)
	v_med3_f32 v0, v16, s73, v188
	v_med3_f32 v7, v17, s73, v188
	v_mov_b32_e32 v9, v1
	v_cvt_pk_fp8_f32 v9, v0, v7
	v_add_u32_e32 v0, 0xc00, v10
	ds_read2_b32 v[10:11], v0 offset0:24 offset1:57
	ds_read2_b32 v[16:17], v0 offset0:90 offset1:123
	s_waitcnt lgkmcnt(2)
	v_med3_f32 v7, v14, s73, v188
	v_med3_f32 v13, v15, s73, v188
	ds_read2_b32 v[14:15], v0 offset0:156 offset1:189
	v_cvt_pk_fp8_f32 v9, v7, v13 op_sel:[0,0,1]
	s_waitcnt lgkmcnt(2)
	v_med3_f32 v7, v10, s73, v188
	v_med3_f32 v11, v11, s73, v188
	s_waitcnt lgkmcnt(1)
	v_med3_f32 v13, v16, s73, v188
	v_med3_f32 v18, v17, s73, v188
	v_mov_b32_e32 v10, v1
	ds_read2_b32 v[16:17], v0 offset0:222 offset1:255
	v_cvt_pk_fp8_f32 v10, v7, v11
	s_waitcnt lgkmcnt(1)
	v_med3_f32 v0, v14, s73, v188
	v_med3_f32 v7, v15, s73, v188
	v_mov_b32_e32 v11, v1
	v_cvt_pk_fp8_f32 v11, v0, v7
	s_waitcnt lgkmcnt(0)
	v_med3_f32 v0, v16, s73, v188
	v_med3_f32 v7, v17, s73, v188
	v_cvt_pk_fp8_f32 v10, v13, v18 op_sel:[0,0,1]
	v_cvt_pk_fp8_f32 v11, v0, v7 op_sel:[0,0,1]
	v_or_b32_e32 v0, s74, v24
	v_lshlrev_b32_e32 v0, 10, v0
	v_lshl_add_u64 v[14:15], s[0:1], 0, v[0:1]
	v_lshl_add_u64 v[14:15], v[14:15], 0, s[8:9]
	v_ashrrev_i32_e32 v13, 31, v12
	v_lshl_add_u64 v[12:13], v[14:15], 0, v[12:13]
	global_store_dwordx4 v[12:13], v[2:5], off
	global_store_dwordx4 v[12:13], v[8:11], off offset:16
	s_waitcnt lgkmcnt(0)
	s_mov_b64 s[0:1], 0
.LBB0_363:
	s_andn2_b64 vcc, exec, s[0:1]
	s_cbranch_vccnz .LBB0_360
	s_lshr_b32 s8, s20, 10
	s_lshl_b64 s[0:1], s[8:9], 23
	s_add_u32 s75, s12, s0
	s_addc_u32 s77, s13, s1
	s_lshl_b64 s[0:1], s[8:9], 21
	s_add_u32 s0, s28, s0
	s_addc_u32 s1, s29, s1
	s_and_b32 s8, s20, 0x3c0
	s_and_b32 s74, s22, 0x7e0
	v_ashrrev_i32_e32 v7, 5, v6
	s_lshl_b32 s76, s74, 2
	v_add_u32_e32 v4, s8, v7
	v_and_b32_e32 v24, 31, v6
	s_add_u32 s76, s75, s76
	v_add_u32_e32 v10, 2, v4
	v_add_u32_e32 v12, 4, v4
	v_add_u32_e32 v14, 6, v4
	v_add_u32_e32 v20, 12, v4
	s_addc_u32 s77, s77, 0
	v_lshlrev_b32_e32 v0, 2, v24
	v_ashrrev_i32_e32 v5, 31, v4
	v_ashrrev_i32_e32 v11, 31, v10
	v_ashrrev_i32_e32 v13, 31, v12
	v_ashrrev_i32_e32 v15, 31, v14
	v_add_u32_e32 v16, 8, v4
	v_add_u32_e32 v18, 10, v4
	v_ashrrev_i32_e32 v21, 31, v20
	v_add_u32_e32 v22, 14, v4
	v_lshl_add_u64 v[2:3], s[76:77], 0, v[0:1]
	v_lshlrev_b64 v[8:9], 13, v[4:5]
	v_lshlrev_b64 v[10:11], 13, v[10:11]
	v_lshlrev_b64 v[12:13], 13, v[12:13]
	v_lshlrev_b64 v[14:15], 13, v[14:15]
	v_ashrrev_i32_e32 v17, 31, v16
	v_ashrrev_i32_e32 v19, 31, v18
	v_lshlrev_b64 v[20:21], 13, v[20:21]
	v_ashrrev_i32_e32 v23, 31, v22
	v_lshl_add_u64 v[8:9], v[2:3], 0, v[8:9]
	v_lshl_add_u64 v[10:11], v[2:3], 0, v[10:11]
	v_lshl_add_u64 v[12:13], v[2:3], 0, v[12:13]
	v_lshl_add_u64 v[14:15], v[2:3], 0, v[14:15]
	v_lshlrev_b64 v[16:17], 13, v[16:17]
	v_lshlrev_b64 v[18:19], 13, v[18:19]
	v_lshl_add_u64 v[20:21], v[2:3], 0, v[20:21]
	v_lshlrev_b64 v[22:23], 13, v[22:23]
	v_lshl_add_u64 v[16:17], v[2:3], 0, v[16:17]
	v_lshl_add_u64 v[18:19], v[2:3], 0, v[18:19]
	v_lshl_add_u64 v[22:23], v[2:3], 0, v[22:23]
	global_load_dword v25, v[8:9], off nt
	global_load_dword v26, v[10:11], off nt
	global_load_dword v27, v[12:13], off nt
	global_load_dword v28, v[14:15], off nt
	global_load_dword v29, v[16:17], off nt
	global_load_dword v30, v[18:19], off nt
	global_load_dword v31, v[20:21], off nt
	global_load_dword v32, v[22:23], off nt
	v_add_u32_e32 v8, 16, v4
	v_add_u32_e32 v10, 18, v4
	v_add_u32_e32 v12, 20, v4
	v_add_u32_e32 v14, 22, v4
	v_add_u32_e32 v20, 28, v4
	v_ashrrev_i32_e32 v9, 31, v8
	v_ashrrev_i32_e32 v11, 31, v10
	v_ashrrev_i32_e32 v13, 31, v12
	v_ashrrev_i32_e32 v15, 31, v14
	v_add_u32_e32 v16, 24, v4
	v_add_u32_e32 v18, 26, v4
	v_ashrrev_i32_e32 v21, 31, v20
	v_add_u32_e32 v22, 30, v4
	v_lshlrev_b64 v[8:9], 13, v[8:9]
	v_lshlrev_b64 v[10:11], 13, v[10:11]
	v_lshlrev_b64 v[12:13], 13, v[12:13]
	v_lshlrev_b64 v[14:15], 13, v[14:15]
	v_ashrrev_i32_e32 v17, 31, v16
	v_ashrrev_i32_e32 v19, 31, v18
	v_lshlrev_b64 v[20:21], 13, v[20:21]
	v_ashrrev_i32_e32 v23, 31, v22
	v_lshl_add_u64 v[8:9], v[2:3], 0, v[8:9]
	v_lshl_add_u64 v[10:11], v[2:3], 0, v[10:11]
	v_lshl_add_u64 v[12:13], v[2:3], 0, v[12:13]
	v_lshl_add_u64 v[14:15], v[2:3], 0, v[14:15]
	v_lshlrev_b64 v[16:17], 13, v[16:17]
	v_lshlrev_b64 v[18:19], 13, v[18:19]
	v_lshl_add_u64 v[20:21], v[2:3], 0, v[20:21]
	v_lshlrev_b64 v[22:23], 13, v[22:23]
	v_lshl_add_u64 v[16:17], v[2:3], 0, v[16:17]
	v_lshl_add_u64 v[18:19], v[2:3], 0, v[18:19]
	v_lshl_add_u64 v[22:23], v[2:3], 0, v[22:23]
	global_load_dword v33, v[8:9], off nt
	global_load_dword v34, v[10:11], off nt
	global_load_dword v35, v[12:13], off nt
	global_load_dword v36, v[14:15], off nt
	global_load_dword v37, v[16:17], off nt
	global_load_dword v38, v[18:19], off nt
	global_load_dword v39, v[20:21], off nt
	global_load_dword v40, v[22:23], off nt
	v_add_u32_e32 v8, 32, v4
	v_add_u32_e32 v10, 34, v4
	v_add_u32_e32 v12, 36, v4
	v_add_u32_e32 v14, 38, v4
	v_add_u32_e32 v20, 44, v4
	v_ashrrev_i32_e32 v9, 31, v8
	v_ashrrev_i32_e32 v11, 31, v10
	v_ashrrev_i32_e32 v13, 31, v12
	v_ashrrev_i32_e32 v15, 31, v14
	v_add_u32_e32 v16, 40, v4
	v_add_u32_e32 v18, 42, v4
	v_ashrrev_i32_e32 v21, 31, v20
	v_add_u32_e32 v22, 46, v4
	v_lshlrev_b64 v[8:9], 13, v[8:9]
	v_lshlrev_b64 v[10:11], 13, v[10:11]
	v_lshlrev_b64 v[12:13], 13, v[12:13]
	v_lshlrev_b64 v[14:15], 13, v[14:15]
	v_ashrrev_i32_e32 v17, 31, v16
	v_ashrrev_i32_e32 v19, 31, v18
	v_lshlrev_b64 v[20:21], 13, v[20:21]
	v_ashrrev_i32_e32 v23, 31, v22
	v_lshl_add_u64 v[8:9], v[2:3], 0, v[8:9]
	v_lshl_add_u64 v[10:11], v[2:3], 0, v[10:11]
	v_lshl_add_u64 v[12:13], v[2:3], 0, v[12:13]
	v_lshl_add_u64 v[14:15], v[2:3], 0, v[14:15]
	v_lshlrev_b64 v[16:17], 13, v[16:17]
	v_lshlrev_b64 v[18:19], 13, v[18:19]
	v_lshl_add_u64 v[20:21], v[2:3], 0, v[20:21]
	v_lshlrev_b64 v[22:23], 13, v[22:23]
	v_lshl_add_u64 v[16:17], v[2:3], 0, v[16:17]
	v_lshl_add_u64 v[18:19], v[2:3], 0, v[18:19]
	v_lshl_add_u64 v[22:23], v[2:3], 0, v[22:23]
	global_load_dword v41, v[8:9], off nt
	global_load_dword v42, v[10:11], off nt
	global_load_dword v43, v[12:13], off nt
	global_load_dword v44, v[14:15], off nt
	global_load_dword v45, v[16:17], off nt
	global_load_dword v46, v[18:19], off nt
	s_nop 0
	global_load_dword v20, v[20:21], off nt
	s_nop 0
	global_load_dword v21, v[22:23], off nt
	v_add_u32_e32 v8, 48, v4
	v_add_u32_e32 v10, 50, v4
	v_add_u32_e32 v12, 52, v4
	v_add_u32_e32 v14, 54, v4
	v_ashrrev_i32_e32 v9, 31, v8
	v_ashrrev_i32_e32 v11, 31, v10
	v_ashrrev_i32_e32 v13, 31, v12
	v_ashrrev_i32_e32 v15, 31, v14
	v_add_u32_e32 v16, 56, v4
	v_add_u32_e32 v18, 58, v4
	v_lshlrev_b64 v[8:9], 13, v[8:9]
	v_lshlrev_b64 v[10:11], 13, v[10:11]
	v_lshlrev_b64 v[12:13], 13, v[12:13]
	v_lshlrev_b64 v[14:15], 13, v[14:15]
	v_ashrrev_i32_e32 v17, 31, v16
	v_ashrrev_i32_e32 v19, 31, v18
	v_lshl_add_u64 v[8:9], v[2:3], 0, v[8:9]
	v_lshl_add_u64 v[10:11], v[2:3], 0, v[10:11]
	v_lshl_add_u64 v[12:13], v[2:3], 0, v[12:13]
	v_lshl_add_u64 v[14:15], v[2:3], 0, v[14:15]
	v_lshlrev_b64 v[16:17], 13, v[16:17]
	v_lshlrev_b64 v[18:19], 13, v[18:19]
	v_lshl_add_u64 v[16:17], v[2:3], 0, v[16:17]
	v_lshl_add_u64 v[18:19], v[2:3], 0, v[18:19]
	global_load_dword v22, v[8:9], off nt
	s_nop 0
	global_load_dword v10, v[10:11], off nt
	s_nop 0
	global_load_dword v11, v[12:13], off nt
	s_nop 0
	global_load_dword v12, v[14:15], off nt
	global_load_dword v13, v[16:17], off nt
	s_nop 0
	global_load_dword v14, v[18:19], off nt
	v_add_u32_e32 v8, 60, v4
	v_ashrrev_i32_e32 v9, 31, v8
	v_add_u32_e32 v4, 62, v4
	v_lshlrev_b64 v[8:9], 13, v[8:9]
	v_ashrrev_i32_e32 v5, 31, v4
	v_lshl_add_u64 v[8:9], v[2:3], 0, v[8:9]
	v_lshlrev_b64 v[4:5], 13, v[4:5]
	v_lshl_add_u64 v[2:3], v[2:3], 0, v[4:5]
	global_load_dword v4, v[8:9], off nt
	global_load_dword v5, v[2:3], off nt
	v_add_u32_e32 v0, s24, v0
	v_mad_u64_u32 v[2:3], s[76:77], v7, s72, v[0:1]
	s_waitcnt vmcnt(0)
	v_mul_f32_e32 v8, 0x42800000, v25
	v_mul_f32_e32 v3, 0x42800000, v26
	ds_write2_b32 v2, v8, v3 offset1:66
	v_mul_f32_e32 v3, 0x42800000, v27
	v_mul_f32_e32 v7, 0x42800000, v28
	ds_write2_b32 v2, v3, v7 offset0:132 offset1:198
	v_mul_f32_e32 v3, 0x42800000, v29
	v_mul_f32_e32 v7, 0x42800000, v30
	v_add_u32_e32 v8, 0x400, v2
	ds_write2_b32 v8, v3, v7 offset0:8 offset1:74
	v_mul_f32_e32 v3, 0x42800000, v31
	v_mul_f32_e32 v7, 0x42800000, v32
	ds_write2_b32 v8, v3, v7 offset0:140 offset1:206
	v_mul_f32_e32 v3, 0x42800000, v33
	v_mul_f32_e32 v7, 0x42800000, v34
	v_add_u32_e32 v8, 0x800, v2
	ds_write2_b32 v8, v3, v7 offset0:16 offset1:82
	v_mul_f32_e32 v3, 0x42800000, v35
	v_mul_f32_e32 v7, 0x42800000, v36
	ds_write2_b32 v8, v3, v7 offset0:148 offset1:214
	v_mul_f32_e32 v3, 0x42800000, v37
	v_mul_f32_e32 v7, 0x42800000, v38
	v_add_u32_e32 v8, 0xc00, v2
	ds_write2_b32 v8, v3, v7 offset0:24 offset1:90
	v_mul_f32_e32 v3, 0x42800000, v39
	v_mul_f32_e32 v7, 0x42800000, v40
	ds_write2_b32 v8, v3, v7 offset0:156 offset1:222
	v_add_u32_e32 v8, 0x1000, v2
	v_mul_f32_e32 v3, 0x42800000, v41
	v_mul_f32_e32 v7, 0x42800000, v42
	ds_write2_b32 v8, v3, v7 offset0:32 offset1:98
	v_mul_f32_e32 v3, 0x42800000, v43
	v_mul_f32_e32 v7, 0x42800000, v44
	ds_write2_b32 v8, v3, v7 offset0:164 offset1:230
	v_mul_f32_e32 v3, 0x42800000, v45
	v_mul_f32_e32 v7, 0x42800000, v46
	v_add_u32_e32 v8, 0x1400, v2
	ds_write2_b32 v8, v3, v7 offset0:40 offset1:106
	v_mul_f32_e32 v3, 0x42800000, v20
	v_mul_f32_e32 v7, 0x42800000, v21
	ds_write2_b32 v8, v3, v7 offset0:172 offset1:238
	v_add_u32_e32 v8, 0x1800, v2
	v_add_u32_e32 v2, 0x1c00, v2
	v_mul_f32_e32 v3, 0x42800000, v22
	v_mul_f32_e32 v7, 0x42800000, v10
	ds_write2_b32 v8, v3, v7 offset0:48 offset1:114
	v_mul_f32_e32 v3, 0x42800000, v11
	v_mul_f32_e32 v7, 0x42800000, v12
	ds_write2_b32 v8, v3, v7 offset0:180 offset1:246
	v_mul_f32_e32 v3, 0x42800000, v13
	v_mul_f32_e32 v7, 0x42800000, v14
	ds_write2_b32 v2, v3, v7 offset0:56 offset1:122
	v_and_b32_e32 v10, 0xffffffe0, v6
	v_mad_u64_u32 v[8:9], s[76:77], v10, s72, v[0:1]
	v_mul_f32_e32 v3, 0x42800000, v4
	v_mul_f32_e32 v4, 0x42800000, v5
	ds_write2_b32 v2, v3, v4 offset0:188 offset1:254
	s_waitcnt lgkmcnt(0)
	ds_read2_b32 v[2:3], v8 offset1:33
	ds_read2_b32 v[4:5], v8 offset0:66 offset1:99
	ds_read2_b32 v[6:7], v8 offset0:132 offset1:165
	s_waitcnt lgkmcnt(2)
	v_med3_f32 v0, v2, s73, v188
	v_med3_f32 v3, v3, s73, v188
	v_mov_b32_e32 v2, v1
	v_cvt_pk_fp8_f32 v2, v0, v3
	s_waitcnt lgkmcnt(1)
	v_med3_f32 v0, v4, s73, v188
	v_med3_f32 v3, v5, s73, v188
	ds_read2_b32 v[4:5], v8 offset0:198 offset1:231
	v_cvt_pk_fp8_f32 v2, v0, v3 op_sel:[0,0,1]
	s_waitcnt lgkmcnt(1)
	v_med3_f32 v0, v6, s73, v188
	v_med3_f32 v6, v7, s73, v188
	v_mov_b32_e32 v3, v1
	v_cvt_pk_fp8_f32 v3, v0, v6
	v_add_u32_e32 v0, 0x400, v8
	ds_read2_b32 v[6:7], v0 offset0:8 offset1:41
	s_waitcnt lgkmcnt(1)
	v_med3_f32 v4, v4, s73, v188
	v_med3_f32 v5, v5, s73, v188
	v_cvt_pk_fp8_f32 v3, v4, v5 op_sel:[0,0,1]
	ds_read2_b32 v[12:13], v0 offset0:74 offset1:107
	s_waitcnt lgkmcnt(1)
	v_med3_f32 v5, v6, s73, v188
	v_med3_f32 v6, v7, s73, v188
	v_mov_b32_e32 v4, v1
	v_cvt_pk_fp8_f32 v4, v5, v6
	ds_read2_b32 v[6:7], v0 offset0:140 offset1:173
	s_waitcnt lgkmcnt(1)
	v_med3_f32 v5, v12, s73, v188
	v_med3_f32 v9, v13, s73, v188
	v_cvt_pk_fp8_f32 v4, v5, v9 op_sel:[0,0,1]
	ds_read2_b32 v[12:13], v0 offset0:206 offset1:239
	s_waitcnt lgkmcnt(1)
	v_med3_f32 v0, v6, s73, v188
	v_med3_f32 v6, v7, s73, v188
	v_mov_b32_e32 v5, v1
	v_cvt_pk_fp8_f32 v5, v0, v6
	v_add_u32_e32 v0, 0x800, v8
	ds_read2_b32 v[6:7], v0 offset0:16 offset1:49
	s_waitcnt lgkmcnt(1)
	v_med3_f32 v9, v12, s73, v188
	v_med3_f32 v11, v13, s73, v188
	ds_read2_b32 v[12:13], v0 offset0:82 offset1:115
	v_cvt_pk_fp8_f32 v5, v9, v11 op_sel:[0,0,1]
	s_waitcnt lgkmcnt(1)
	v_med3_f32 v9, v6, s73, v188
	v_med3_f32 v7, v7, s73, v188
	v_mov_b32_e32 v6, v1
	ds_read2_b32 v[14:15], v0 offset0:148 offset1:181
	v_cvt_pk_fp8_f32 v6, v9, v7
	s_waitcnt lgkmcnt(1)
	v_med3_f32 v7, v12, s73, v188
	v_med3_f32 v9, v13, s73, v188
	ds_read2_b32 v[12:13], v0 offset0:214 offset1:247
	v_cvt_pk_fp8_f32 v6, v7, v9 op_sel:[0,0,1]
	s_waitcnt lgkmcnt(1)
	v_med3_f32 v0, v14, s73, v188
	v_med3_f32 v9, v15, s73, v188
	v_mov_b32_e32 v7, v1
	v_cvt_pk_fp8_f32 v7, v0, v9
	v_add_u32_e32 v0, 0xc00, v8
	ds_read2_b32 v[8:9], v0 offset0:24 offset1:57
	s_waitcnt lgkmcnt(1)
	v_med3_f32 v11, v12, s73, v188
	ds_read2_b32 v[14:15], v0 offset0:90 offset1:123
	v_med3_f32 v12, v13, s73, v188
	v_cvt_pk_fp8_f32 v7, v11, v12 op_sel:[0,0,1]
	ds_read2_b32 v[12:13], v0 offset0:156 offset1:189
	s_waitcnt lgkmcnt(2)
	v_med3_f32 v11, v8, s73, v188
	v_med3_f32 v9, v9, s73, v188
	s_waitcnt lgkmcnt(1)
	v_med3_f32 v16, v14, s73, v188
	v_med3_f32 v17, v15, s73, v188
	v_mov_b32_e32 v8, v1
	ds_read2_b32 v[14:15], v0 offset0:222 offset1:255
	v_cvt_pk_fp8_f32 v8, v11, v9
	s_waitcnt lgkmcnt(1)
	v_med3_f32 v0, v12, s73, v188
	v_med3_f32 v11, v13, s73, v188
	v_mov_b32_e32 v9, v1
	v_cvt_pk_fp8_f32 v9, v0, v11
	s_waitcnt lgkmcnt(0)
	v_med3_f32 v0, v14, s73, v188
	v_med3_f32 v11, v15, s73, v188
	v_cvt_pk_fp8_f32 v8, v16, v17 op_sel:[0,0,1]
	v_cvt_pk_fp8_f32 v9, v0, v11 op_sel:[0,0,1]
	v_or_b32_e32 v0, s74, v24
	v_lshlrev_b32_e32 v0, 10, v0
	v_lshl_add_u64 v[12:13], s[0:1], 0, v[0:1]
	v_lshl_add_u64 v[12:13], v[12:13], 0, s[8:9]
	v_ashrrev_i32_e32 v11, 31, v10
	v_lshl_add_u64 v[10:11], v[12:13], 0, v[10:11]
	global_store_dwordx4 v[10:11], v[2:5], off
	global_store_dwordx4 v[10:11], v[6:9], off offset:16
	s_waitcnt lgkmcnt(0)
	s_branch .LBB0_360

.LBB0_1473:
	v_mov_b32_e32 v6, v158
	s_cmp_gt_i32 s15, 0xbfff
	s_cbranch_scc1 .LBB0_1472
	s_cmpk_gt_i32 s15, 0x7fff
	s_mov_b64 s[2:3], -1
	s_cbranch_scc0 .LBB0_1476
	s_add_i32 s2, s15, 0xffff8000
	s_lshr_b32 s6, s2, 9
	s_lshl_b64 s[2:3], s[6:7], 20
	s_lshl_b64 s[18:19], s[6:7], 22
	s_add_u32 s20, s12, s18
	s_addc_u32 s19, s13, s19
	s_add_u32 s2, s33, s2
	s_addc_u32 s3, s34, s3
	s_and_b32 s6, s17, 0x3c0
	s_and_b32 s18, s44, 0x3e0
	v_ashrrev_i32_e32 v7, 5, v6
	s_lshl_b32 s21, s18, 2
	v_add_u32_e32 v4, s6, v7
	v_and_b32_e32 v24, 31, v6
	s_add_u32 s20, s20, s21
	v_add_u32_e32 v10, 2, v4
	v_add_u32_e32 v12, 4, v4
	v_add_u32_e32 v14, 6, v4
	v_add_u32_e32 v20, 12, v4
	s_addc_u32 s21, s19, 0
	v_lshlrev_b32_e32 v0, 2, v24
	v_ashrrev_i32_e32 v5, 31, v4
	v_ashrrev_i32_e32 v11, 31, v10
	v_ashrrev_i32_e32 v13, 31, v12
	v_ashrrev_i32_e32 v15, 31, v14
	v_add_u32_e32 v16, 8, v4
	v_add_u32_e32 v18, 10, v4
	v_ashrrev_i32_e32 v21, 31, v20
	v_add_u32_e32 v22, 14, v4
	v_lshl_add_u64 v[2:3], s[20:21], 0, v[0:1]
	v_lshlrev_b64 v[8:9], 12, v[4:5]
	v_lshlrev_b64 v[10:11], 12, v[10:11]
	v_lshlrev_b64 v[12:13], 12, v[12:13]
	v_lshlrev_b64 v[14:15], 12, v[14:15]
	v_ashrrev_i32_e32 v17, 31, v16
	v_ashrrev_i32_e32 v19, 31, v18
	v_lshlrev_b64 v[20:21], 12, v[20:21]
	v_ashrrev_i32_e32 v23, 31, v22
	v_lshl_add_u64 v[8:9], v[2:3], 0, v[8:9]
	v_lshl_add_u64 v[10:11], v[2:3], 0, v[10:11]
	v_lshl_add_u64 v[12:13], v[2:3], 0, v[12:13]
	v_lshl_add_u64 v[14:15], v[2:3], 0, v[14:15]
	v_lshlrev_b64 v[16:17], 12, v[16:17]
	v_lshlrev_b64 v[18:19], 12, v[18:19]
	v_lshl_add_u64 v[20:21], v[2:3], 0, v[20:21]
	v_lshlrev_b64 v[22:23], 12, v[22:23]
	v_lshl_add_u64 v[16:17], v[2:3], 0, v[16:17]
	v_lshl_add_u64 v[18:19], v[2:3], 0, v[18:19]
	v_lshl_add_u64 v[22:23], v[2:3], 0, v[22:23]
	global_load_dword v25, v[8:9], off nt
	global_load_dword v26, v[10:11], off nt
	global_load_dword v27, v[12:13], off nt
	global_load_dword v28, v[14:15], off nt
	global_load_dword v29, v[16:17], off nt
	global_load_dword v30, v[18:19], off nt
	global_load_dword v31, v[20:21], off nt
	global_load_dword v32, v[22:23], off nt
	v_add_u32_e32 v8, 16, v4
	v_add_u32_e32 v10, 18, v4
	v_add_u32_e32 v12, 20, v4
	v_add_u32_e32 v14, 22, v4
	v_add_u32_e32 v20, 28, v4
	v_ashrrev_i32_e32 v9, 31, v8
	v_ashrrev_i32_e32 v11, 31, v10
	v_ashrrev_i32_e32 v13, 31, v12
	v_ashrrev_i32_e32 v15, 31, v14
	v_add_u32_e32 v16, 24, v4
	v_add_u32_e32 v18, 26, v4
	v_ashrrev_i32_e32 v21, 31, v20
	v_add_u32_e32 v22, 30, v4
	v_lshlrev_b64 v[8:9], 12, v[8:9]
	v_lshlrev_b64 v[10:11], 12, v[10:11]
	v_lshlrev_b64 v[12:13], 12, v[12:13]
	v_lshlrev_b64 v[14:15], 12, v[14:15]
	v_ashrrev_i32_e32 v17, 31, v16
	v_ashrrev_i32_e32 v19, 31, v18
	v_lshlrev_b64 v[20:21], 12, v[20:21]
	v_ashrrev_i32_e32 v23, 31, v22
	v_lshl_add_u64 v[8:9], v[2:3], 0, v[8:9]
	v_lshl_add_u64 v[10:11], v[2:3], 0, v[10:11]
	v_lshl_add_u64 v[12:13], v[2:3], 0, v[12:13]
	v_lshl_add_u64 v[14:15], v[2:3], 0, v[14:15]
	v_lshlrev_b64 v[16:17], 12, v[16:17]
	v_lshlrev_b64 v[18:19], 12, v[18:19]
	v_lshl_add_u64 v[20:21], v[2:3], 0, v[20:21]
	v_lshlrev_b64 v[22:23], 12, v[22:23]
	v_lshl_add_u64 v[16:17], v[2:3], 0, v[16:17]
	v_lshl_add_u64 v[18:19], v[2:3], 0, v[18:19]
	v_lshl_add_u64 v[22:23], v[2:3], 0, v[22:23]
	global_load_dword v33, v[8:9], off nt
	global_load_dword v34, v[10:11], off nt
	global_load_dword v35, v[12:13], off nt
	global_load_dword v36, v[14:15], off nt
	global_load_dword v37, v[16:17], off nt
	global_load_dword v38, v[18:19], off nt
	global_load_dword v39, v[20:21], off nt
	global_load_dword v40, v[22:23], off nt
	v_add_u32_e32 v8, 32, v4
	v_add_u32_e32 v10, 34, v4
	v_add_u32_e32 v12, 36, v4
	v_add_u32_e32 v14, 38, v4
	v_add_u32_e32 v20, 44, v4
	v_ashrrev_i32_e32 v9, 31, v8
	v_ashrrev_i32_e32 v11, 31, v10
	v_ashrrev_i32_e32 v13, 31, v12
	v_ashrrev_i32_e32 v15, 31, v14
	v_add_u32_e32 v16, 40, v4
	v_add_u32_e32 v18, 42, v4
	v_ashrrev_i32_e32 v21, 31, v20
	v_add_u32_e32 v22, 46, v4
	v_lshlrev_b64 v[8:9], 12, v[8:9]
	v_lshlrev_b64 v[10:11], 12, v[10:11]
	v_lshlrev_b64 v[12:13], 12, v[12:13]
	v_lshlrev_b64 v[14:15], 12, v[14:15]
	v_ashrrev_i32_e32 v17, 31, v16
	v_ashrrev_i32_e32 v19, 31, v18
	v_lshlrev_b64 v[20:21], 12, v[20:21]
	v_ashrrev_i32_e32 v23, 31, v22
	v_lshl_add_u64 v[8:9], v[2:3], 0, v[8:9]
	v_lshl_add_u64 v[10:11], v[2:3], 0, v[10:11]
	v_lshl_add_u64 v[12:13], v[2:3], 0, v[12:13]
	v_lshl_add_u64 v[14:15], v[2:3], 0, v[14:15]
	v_lshlrev_b64 v[16:17], 12, v[16:17]
	v_lshlrev_b64 v[18:19], 12, v[18:19]
	v_lshl_add_u64 v[20:21], v[2:3], 0, v[20:21]
	v_lshlrev_b64 v[22:23], 12, v[22:23]
	v_lshl_add_u64 v[16:17], v[2:3], 0, v[16:17]
	v_lshl_add_u64 v[18:19], v[2:3], 0, v[18:19]
	v_lshl_add_u64 v[22:23], v[2:3], 0, v[22:23]
	global_load_dword v41, v[8:9], off nt
	global_load_dword v42, v[10:11], off nt
	global_load_dword v43, v[12:13], off nt
	global_load_dword v44, v[14:15], off nt
	global_load_dword v45, v[16:17], off nt
	global_load_dword v46, v[18:19], off nt
	s_nop 0
	global_load_dword v20, v[20:21], off nt
	s_nop 0
	global_load_dword v21, v[22:23], off nt
	v_add_u32_e32 v8, 48, v4
	v_add_u32_e32 v10, 50, v4
	v_add_u32_e32 v12, 52, v4
	v_add_u32_e32 v14, 54, v4
	v_ashrrev_i32_e32 v9, 31, v8
	v_ashrrev_i32_e32 v11, 31, v10
	v_ashrrev_i32_e32 v13, 31, v12
	v_ashrrev_i32_e32 v15, 31, v14
	v_add_u32_e32 v16, 56, v4
	v_add_u32_e32 v18, 58, v4
	v_lshlrev_b64 v[8:9], 12, v[8:9]
	v_lshlrev_b64 v[10:11], 12, v[10:11]
	v_lshlrev_b64 v[12:13], 12, v[12:13]
	v_lshlrev_b64 v[14:15], 12, v[14:15]
	v_ashrrev_i32_e32 v17, 31, v16
	v_ashrrev_i32_e32 v19, 31, v18
	v_lshl_add_u64 v[8:9], v[2:3], 0, v[8:9]
	v_lshl_add_u64 v[10:11], v[2:3], 0, v[10:11]
	v_lshl_add_u64 v[12:13], v[2:3], 0, v[12:13]
	v_lshl_add_u64 v[14:15], v[2:3], 0, v[14:15]
	v_lshlrev_b64 v[16:17], 12, v[16:17]
	v_lshlrev_b64 v[18:19], 12, v[18:19]
	v_lshl_add_u64 v[16:17], v[2:3], 0, v[16:17]
	v_lshl_add_u64 v[18:19], v[2:3], 0, v[18:19]
	global_load_dword v22, v[8:9], off nt
	s_nop 0
	global_load_dword v10, v[10:11], off nt
	s_nop 0
	global_load_dword v11, v[12:13], off nt
	s_nop 0
	global_load_dword v12, v[14:15], off nt
	global_load_dword v13, v[16:17], off nt
	s_nop 0
	global_load_dword v14, v[18:19], off nt
	v_add_u32_e32 v8, 60, v4
	v_ashrrev_i32_e32 v9, 31, v8
	v_add_u32_e32 v4, 62, v4
	v_lshlrev_b64 v[8:9], 12, v[8:9]
	v_ashrrev_i32_e32 v5, 31, v4
	v_lshl_add_u64 v[8:9], v[2:3], 0, v[8:9]
	v_lshlrev_b64 v[4:5], 12, v[4:5]
	v_lshl_add_u64 v[2:3], v[2:3], 0, v[4:5]
	global_load_dword v4, v[8:9], off nt
	global_load_dword v5, v[2:3], off nt
	v_add_u32_e32 v0, s23, v0
	v_mad_u64_u32 v[2:3], s[20:21], v7, s40, v[0:1]
	s_waitcnt vmcnt(31)
	v_mul_f32_e32 v8, 0x42800000, v25
	s_waitcnt vmcnt(30)
	v_mul_f32_e32 v3, 0x42800000, v26
	ds_write2_b32 v2, v8, v3 offset1:66
	s_waitcnt vmcnt(29)
	v_mul_f32_e32 v3, 0x42800000, v27
	s_waitcnt vmcnt(28)
	v_mul_f32_e32 v7, 0x42800000, v28
	ds_write2_b32 v2, v3, v7 offset0:132 offset1:198
	s_waitcnt vmcnt(27)
	v_mul_f32_e32 v3, 0x42800000, v29
	s_waitcnt vmcnt(26)
	v_mul_f32_e32 v7, 0x42800000, v30
	v_add_u32_e32 v8, 0x400, v2
	ds_write2_b32 v8, v3, v7 offset0:8 offset1:74
	s_waitcnt vmcnt(25)
	v_mul_f32_e32 v3, 0x42800000, v31
	s_waitcnt vmcnt(24)
	v_mul_f32_e32 v7, 0x42800000, v32
	ds_write2_b32 v8, v3, v7 offset0:140 offset1:206
	s_waitcnt vmcnt(23)
	v_mul_f32_e32 v3, 0x42800000, v33
	s_waitcnt vmcnt(22)
	v_mul_f32_e32 v7, 0x42800000, v34
	v_add_u32_e32 v8, 0x800, v2
	ds_write2_b32 v8, v3, v7 offset0:16 offset1:82
	s_waitcnt vmcnt(21)
	v_mul_f32_e32 v3, 0x42800000, v35
	s_waitcnt vmcnt(20)
	v_mul_f32_e32 v7, 0x42800000, v36
	ds_write2_b32 v8, v3, v7 offset0:148 offset1:214
	s_waitcnt vmcnt(19)
	v_mul_f32_e32 v3, 0x42800000, v37
	s_waitcnt vmcnt(18)
	v_mul_f32_e32 v7, 0x42800000, v38
	v_add_u32_e32 v8, 0xc00, v2
	ds_write2_b32 v8, v3, v7 offset0:24 offset1:90
	s_waitcnt vmcnt(17)
	v_mul_f32_e32 v3, 0x42800000, v39
	s_waitcnt vmcnt(16)
	v_mul_f32_e32 v7, 0x42800000, v40
	ds_write2_b32 v8, v3, v7 offset0:156 offset1:222
	v_add_u32_e32 v8, 0x1000, v2
	s_waitcnt vmcnt(15)
	v_mul_f32_e32 v3, 0x42800000, v41
	s_waitcnt vmcnt(14)
	v_mul_f32_e32 v7, 0x42800000, v42
	ds_write2_b32 v8, v3, v7 offset0:32 offset1:98
	s_waitcnt vmcnt(13)
	v_mul_f32_e32 v3, 0x42800000, v43
	s_waitcnt vmcnt(12)
	v_mul_f32_e32 v7, 0x42800000, v44
	ds_write2_b32 v8, v3, v7 offset0:164 offset1:230
	s_waitcnt vmcnt(11)
	v_mul_f32_e32 v3, 0x42800000, v45
	s_waitcnt vmcnt(10)
	v_mul_f32_e32 v7, 0x42800000, v46
	v_add_u32_e32 v8, 0x1400, v2
	ds_write2_b32 v8, v3, v7 offset0:40 offset1:106
	s_waitcnt vmcnt(9)
	v_mul_f32_e32 v3, 0x42800000, v20
	s_waitcnt vmcnt(8)
	v_mul_f32_e32 v7, 0x42800000, v21
	ds_write2_b32 v8, v3, v7 offset0:172 offset1:238
	v_add_u32_e32 v8, 0x1800, v2
	v_add_u32_e32 v2, 0x1c00, v2
	s_waitcnt vmcnt(7)
	v_mul_f32_e32 v3, 0x42800000, v22
	s_waitcnt vmcnt(6)
	v_mul_f32_e32 v7, 0x42800000, v10
	ds_write2_b32 v8, v3, v7 offset0:48 offset1:114
	s_waitcnt vmcnt(5)
	v_mul_f32_e32 v3, 0x42800000, v11
	s_waitcnt vmcnt(4)
	v_mul_f32_e32 v7, 0x42800000, v12
	ds_write2_b32 v8, v3, v7 offset0:180 offset1:246
	s_waitcnt vmcnt(3)
	v_mul_f32_e32 v3, 0x42800000, v13
	s_waitcnt vmcnt(2)
	v_mul_f32_e32 v7, 0x42800000, v14
	ds_write2_b32 v2, v3, v7 offset0:56 offset1:122
	v_and_b32_e32 v12, 0xffffffe0, v6
	v_mad_u64_u32 v[10:11], s[20:21], v12, s40, v[0:1]
	s_waitcnt vmcnt(1)
	v_mul_f32_e32 v3, 0x42800000, v4
	s_waitcnt vmcnt(0)
	v_mul_f32_e32 v4, 0x42800000, v5
	ds_write2_b32 v2, v3, v4 offset0:188 offset1:254
	s_waitcnt lgkmcnt(0)
	ds_read2_b32 v[2:3], v10 offset1:33
	ds_read2_b32 v[4:5], v10 offset0:66 offset1:99
	ds_read2_b32 v[8:9], v10 offset0:132 offset1:165
	s_waitcnt lgkmcnt(2)
	v_med3_f32 v0, v2, s39, v162
	v_med3_f32 v3, v3, s39, v162
	v_mov_b32_e32 v2, v1
	v_cvt_pk_fp8_f32 v2, v0, v3
	s_waitcnt lgkmcnt(1)
	v_med3_f32 v0, v4, s39, v162
	v_med3_f32 v3, v5, s39, v162
	s_waitcnt lgkmcnt(0)
	v_med3_f32 v7, v9, s39, v162
	v_cvt_pk_fp8_f32 v2, v0, v3 op_sel:[0,0,1]
	v_med3_f32 v0, v8, s39, v162
	v_mov_b32_e32 v3, v1
	ds_read2_b32 v[4:5], v10 offset0:198 offset1:231
	v_cvt_pk_fp8_f32 v3, v0, v7
	v_add_u32_e32 v0, 0x400, v10
	ds_read2_b32 v[8:9], v0 offset0:8 offset1:41
	ds_read2_b32 v[14:15], v0 offset0:74 offset1:107
	s_waitcnt lgkmcnt(2)
	v_med3_f32 v4, v4, s39, v162
	v_med3_f32 v5, v5, s39, v162
	v_cvt_pk_fp8_f32 v3, v4, v5 op_sel:[0,0,1]
	s_waitcnt lgkmcnt(1)
	v_med3_f32 v5, v8, s39, v162
	v_med3_f32 v7, v9, s39, v162
	v_mov_b32_e32 v4, v1
	ds_read2_b32 v[8:9], v0 offset0:140 offset1:173
	v_cvt_pk_fp8_f32 v4, v5, v7
	s_waitcnt lgkmcnt(1)
	v_med3_f32 v5, v14, s39, v162
	v_med3_f32 v7, v15, s39, v162
	ds_read2_b32 v[14:15], v0 offset0:206 offset1:239
	v_cvt_pk_fp8_f32 v4, v5, v7 op_sel:[0,0,1]
	s_waitcnt lgkmcnt(1)
	v_med3_f32 v0, v8, s39, v162
	v_med3_f32 v7, v9, s39, v162
	v_mov_b32_e32 v5, v1
	v_cvt_pk_fp8_f32 v5, v0, v7
	v_add_u32_e32 v0, 0x800, v10
	ds_read2_b32 v[8:9], v0 offset0:16 offset1:49
	s_waitcnt lgkmcnt(1)
	v_med3_f32 v7, v14, s39, v162
	v_med3_f32 v11, v15, s39, v162
	ds_read2_b32 v[14:15], v0 offset0:82 offset1:115
	v_cvt_pk_fp8_f32 v5, v7, v11 op_sel:[0,0,1]
	s_waitcnt lgkmcnt(1)
	v_med3_f32 v7, v8, s39, v162
	v_med3_f32 v9, v9, s39, v162
	v_mov_b32_e32 v8, v1
	ds_read2_b32 v[16:17], v0 offset0:148 offset1:181
	v_cvt_pk_fp8_f32 v8, v7, v9
	s_waitcnt lgkmcnt(1)
	v_med3_f32 v7, v14, s39, v162
	v_med3_f32 v9, v15, s39, v162
	ds_read2_b32 v[14:15], v0 offset0:214 offset1:247
	v_cvt_pk_fp8_f32 v8, v7, v9 op_sel:[0,0,1]
	s_waitcnt lgkmcnt(1)
	v_med3_f32 v0, v16, s39, v162
	v_med3_f32 v7, v17, s39, v162
	v_mov_b32_e32 v9, v1
	v_cvt_pk_fp8_f32 v9, v0, v7
	v_add_u32_e32 v0, 0xc00, v10
	ds_read2_b32 v[10:11], v0 offset0:24 offset1:57
	ds_read2_b32 v[16:17], v0 offset0:90 offset1:123
	s_waitcnt lgkmcnt(2)
	v_med3_f32 v7, v14, s39, v162
	v_med3_f32 v13, v15, s39, v162
	ds_read2_b32 v[14:15], v0 offset0:156 offset1:189
	v_cvt_pk_fp8_f32 v9, v7, v13 op_sel:[0,0,1]
	s_waitcnt lgkmcnt(2)
	v_med3_f32 v7, v10, s39, v162
	v_med3_f32 v11, v11, s39, v162
	s_waitcnt lgkmcnt(1)
	v_med3_f32 v13, v16, s39, v162
	v_med3_f32 v18, v17, s39, v162
	v_mov_b32_e32 v10, v1
	ds_read2_b32 v[16:17], v0 offset0:222 offset1:255
	v_cvt_pk_fp8_f32 v10, v7, v11
	s_waitcnt lgkmcnt(1)
	v_med3_f32 v0, v14, s39, v162
	v_med3_f32 v7, v15, s39, v162
	v_mov_b32_e32 v11, v1
	v_cvt_pk_fp8_f32 v11, v0, v7
	s_waitcnt lgkmcnt(0)
	v_med3_f32 v0, v16, s39, v162
	v_med3_f32 v7, v17, s39, v162
	v_cvt_pk_fp8_f32 v10, v13, v18 op_sel:[0,0,1]
	v_cvt_pk_fp8_f32 v11, v0, v7 op_sel:[0,0,1]
	v_or_b32_e32 v0, s18, v24
	v_lshlrev_b32_e32 v0, 10, v0
	v_lshl_add_u64 v[14:15], s[2:3], 0, v[0:1]
	v_lshl_add_u64 v[14:15], v[14:15], 0, s[6:7]
	v_ashrrev_i32_e32 v13, 31, v12
	v_lshl_add_u64 v[12:13], v[14:15], 0, v[12:13]
	global_store_dwordx4 v[12:13], v[2:5], off
	global_store_dwordx4 v[12:13], v[8:11], off offset:16
	s_waitcnt lgkmcnt(0)
	s_mov_b64 s[2:3], 0
.LBB0_1476:
	s_andn2_b64 vcc, exec, s[2:3]
	s_cbranch_vccnz .LBB0_1472
	s_ashr_i32 s2, s15, 31
	s_lshr_b32 s2, s2, 22
	s_add_i32 s3, s15, s2
	s_ashr_i32 s2, s3, 10
	s_and_b32 s3, s3, 0xfc00
	s_sub_i32 s6, s15, s3
	s_ashr_i32 s3, s2, 31
	s_lshl_b64 s[18:19], s[2:3], 23
	s_add_u32 s48, s10, s18
	s_addc_u32 s19, s11, s19
	s_lshl_b64 s[2:3], s[2:3], 21
	s_add_u32 s2, s35, s2
	s_sext_i32_i16 s18, s6
	s_addc_u32 s3, s36, s3
	s_bfe_u32 s18, s18, 0x60019
	s_add_i32 s18, s6, s18
	s_sext_i32_i16 s20, s18
	s_and_b32 s18, s18, 0xffc0
	s_sub_i32 s6, s6, s18
	s_sext_i32_i16 s6, s6
	s_and_b32 s18, s20, 0xffffffc0
	s_lshl_b32 s20, s6, 5
	v_ashrrev_i32_e32 v7, 5, v6
	s_ashr_i32 s21, s20, 31
	s_lshl_b64 s[46:47], s[20:21], 2
	v_add_u32_e32 v4, s18, v7
	v_and_b32_e32 v24, 31, v6
	s_add_u32 s46, s48, s46
	v_add_u32_e32 v10, 2, v4
	v_add_u32_e32 v12, 4, v4
	v_add_u32_e32 v14, 6, v4
	v_add_u32_e32 v20, 12, v4
	s_addc_u32 s47, s19, s47
	v_lshlrev_b32_e32 v0, 2, v24
	v_ashrrev_i32_e32 v5, 31, v4
	v_ashrrev_i32_e32 v11, 31, v10
	v_ashrrev_i32_e32 v13, 31, v12
	v_ashrrev_i32_e32 v15, 31, v14
	v_add_u32_e32 v16, 8, v4
	v_add_u32_e32 v18, 10, v4
	v_ashrrev_i32_e32 v21, 31, v20
	v_add_u32_e32 v22, 14, v4
	v_lshl_add_u64 v[2:3], s[46:47], 0, v[0:1]
	v_lshlrev_b64 v[8:9], 13, v[4:5]
	v_lshlrev_b64 v[10:11], 13, v[10:11]
	v_lshlrev_b64 v[12:13], 13, v[12:13]
	v_lshlrev_b64 v[14:15], 13, v[14:15]
	v_ashrrev_i32_e32 v17, 31, v16
	v_ashrrev_i32_e32 v19, 31, v18
	v_lshlrev_b64 v[20:21], 13, v[20:21]
	v_ashrrev_i32_e32 v23, 31, v22
	v_lshl_add_u64 v[8:9], v[2:3], 0, v[8:9]
	v_lshl_add_u64 v[10:11], v[2:3], 0, v[10:11]
	v_lshl_add_u64 v[12:13], v[2:3], 0, v[12:13]
	v_lshl_add_u64 v[14:15], v[2:3], 0, v[14:15]
	v_lshlrev_b64 v[16:17], 13, v[16:17]
	v_lshlrev_b64 v[18:19], 13, v[18:19]
	v_lshl_add_u64 v[20:21], v[2:3], 0, v[20:21]
	v_lshlrev_b64 v[22:23], 13, v[22:23]
	v_lshl_add_u64 v[16:17], v[2:3], 0, v[16:17]
	v_lshl_add_u64 v[18:19], v[2:3], 0, v[18:19]
	v_lshl_add_u64 v[22:23], v[2:3], 0, v[22:23]
	global_load_dword v25, v[8:9], off nt
	global_load_dword v26, v[10:11], off nt
	global_load_dword v27, v[12:13], off nt
	global_load_dword v28, v[14:15], off nt
	global_load_dword v29, v[16:17], off nt
	global_load_dword v30, v[18:19], off nt
	global_load_dword v31, v[20:21], off nt
	global_load_dword v32, v[22:23], off nt
	v_add_u32_e32 v8, 16, v4
	v_add_u32_e32 v10, 18, v4
	v_add_u32_e32 v12, 20, v4
	v_add_u32_e32 v14, 22, v4
	v_add_u32_e32 v20, 28, v4
	v_ashrrev_i32_e32 v9, 31, v8
	v_ashrrev_i32_e32 v11, 31, v10
	v_ashrrev_i32_e32 v13, 31, v12
	v_ashrrev_i32_e32 v15, 31, v14
	v_add_u32_e32 v16, 24, v4
	v_add_u32_e32 v18, 26, v4
	v_ashrrev_i32_e32 v21, 31, v20
	v_add_u32_e32 v22, 30, v4
	v_lshlrev_b64 v[8:9], 13, v[8:9]
	v_lshlrev_b64 v[10:11], 13, v[10:11]
	v_lshlrev_b64 v[12:13], 13, v[12:13]
	v_lshlrev_b64 v[14:15], 13, v[14:15]
	v_ashrrev_i32_e32 v17, 31, v16
	v_ashrrev_i32_e32 v19, 31, v18
	v_lshlrev_b64 v[20:21], 13, v[20:21]
	v_ashrrev_i32_e32 v23, 31, v22
	v_lshl_add_u64 v[8:9], v[2:3], 0, v[8:9]
	v_lshl_add_u64 v[10:11], v[2:3], 0, v[10:11]
	v_lshl_add_u64 v[12:13], v[2:3], 0, v[12:13]
	v_lshl_add_u64 v[14:15], v[2:3], 0, v[14:15]
	v_lshlrev_b64 v[16:17], 13, v[16:17]
	v_lshlrev_b64 v[18:19], 13, v[18:19]
	v_lshl_add_u64 v[20:21], v[2:3], 0, v[20:21]
	v_lshlrev_b64 v[22:23], 13, v[22:23]
	v_lshl_add_u64 v[16:17], v[2:3], 0, v[16:17]
	v_lshl_add_u64 v[18:19], v[2:3], 0, v[18:19]
	v_lshl_add_u64 v[22:23], v[2:3], 0, v[22:23]
	global_load_dword v33, v[8:9], off nt
	global_load_dword v34, v[10:11], off nt
	global_load_dword v35, v[12:13], off nt
	global_load_dword v36, v[14:15], off nt
	global_load_dword v37, v[16:17], off nt
	global_load_dword v38, v[18:19], off nt
	global_load_dword v39, v[20:21], off nt
	global_load_dword v40, v[22:23], off nt
	v_add_u32_e32 v8, 32, v4
	v_add_u32_e32 v10, 34, v4
	v_add_u32_e32 v12, 36, v4
	v_add_u32_e32 v14, 38, v4
	v_add_u32_e32 v20, 44, v4
	v_ashrrev_i32_e32 v9, 31, v8
	v_ashrrev_i32_e32 v11, 31, v10
	v_ashrrev_i32_e32 v13, 31, v12
	v_ashrrev_i32_e32 v15, 31, v14
	v_add_u32_e32 v16, 40, v4
	v_add_u32_e32 v18, 42, v4
	v_ashrrev_i32_e32 v21, 31, v20
	v_add_u32_e32 v22, 46, v4
	v_lshlrev_b64 v[8:9], 13, v[8:9]
	v_lshlrev_b64 v[10:11], 13, v[10:11]
	v_lshlrev_b64 v[12:13], 13, v[12:13]
	v_lshlrev_b64 v[14:15], 13, v[14:15]
	v_ashrrev_i32_e32 v17, 31, v16
	v_ashrrev_i32_e32 v19, 31, v18
	v_lshlrev_b64 v[20:21], 13, v[20:21]
	v_ashrrev_i32_e32 v23, 31, v22
	v_lshl_add_u64 v[8:9], v[2:3], 0, v[8:9]
	v_lshl_add_u64 v[10:11], v[2:3], 0, v[10:11]
	v_lshl_add_u64 v[12:13], v[2:3], 0, v[12:13]
	v_lshl_add_u64 v[14:15], v[2:3], 0, v[14:15]
	v_lshlrev_b64 v[16:17], 13, v[16:17]
	v_lshlrev_b64 v[18:19], 13, v[18:19]
	v_lshl_add_u64 v[20:21], v[2:3], 0, v[20:21]
	v_lshlrev_b64 v[22:23], 13, v[22:23]
	v_lshl_add_u64 v[16:17], v[2:3], 0, v[16:17]
	v_lshl_add_u64 v[18:19], v[2:3], 0, v[18:19]
	v_lshl_add_u64 v[22:23], v[2:3], 0, v[22:23]
	global_load_dword v41, v[8:9], off nt
	global_load_dword v42, v[10:11], off nt
	global_load_dword v43, v[12:13], off nt
	global_load_dword v44, v[14:15], off nt
	global_load_dword v45, v[16:17], off nt
	global_load_dword v46, v[18:19], off nt
	s_nop 0
	global_load_dword v20, v[20:21], off nt
	s_nop 0
	global_load_dword v21, v[22:23], off nt
	v_add_u32_e32 v8, 48, v4
	v_add_u32_e32 v10, 50, v4
	v_add_u32_e32 v12, 52, v4
	v_add_u32_e32 v14, 54, v4
	v_ashrrev_i32_e32 v9, 31, v8
	v_ashrrev_i32_e32 v11, 31, v10
	v_ashrrev_i32_e32 v13, 31, v12
	v_ashrrev_i32_e32 v15, 31, v14
	v_add_u32_e32 v16, 56, v4
	v_add_u32_e32 v18, 58, v4
	v_lshlrev_b64 v[8:9], 13, v[8:9]
	v_lshlrev_b64 v[10:11], 13, v[10:11]
	v_lshlrev_b64 v[12:13], 13, v[12:13]
	v_lshlrev_b64 v[14:15], 13, v[14:15]
	v_ashrrev_i32_e32 v17, 31, v16
	v_ashrrev_i32_e32 v19, 31, v18
	v_lshl_add_u64 v[8:9], v[2:3], 0, v[8:9]
	v_lshl_add_u64 v[10:11], v[2:3], 0, v[10:11]
	v_lshl_add_u64 v[12:13], v[2:3], 0, v[12:13]
	v_lshl_add_u64 v[14:15], v[2:3], 0, v[14:15]
	v_lshlrev_b64 v[16:17], 13, v[16:17]
	v_lshlrev_b64 v[18:19], 13, v[18:19]
	v_lshl_add_u64 v[16:17], v[2:3], 0, v[16:17]
	v_lshl_add_u64 v[18:19], v[2:3], 0, v[18:19]
	global_load_dword v22, v[8:9], off nt
	s_nop 0
	global_load_dword v10, v[10:11], off nt
	s_nop 0
	global_load_dword v11, v[12:13], off nt
	s_nop 0
	global_load_dword v12, v[14:15], off nt
	global_load_dword v13, v[16:17], off nt
	s_nop 0
	global_load_dword v14, v[18:19], off nt
	v_add_u32_e32 v8, 60, v4
	v_ashrrev_i32_e32 v9, 31, v8
	v_add_u32_e32 v4, 62, v4
	v_lshlrev_b64 v[8:9], 13, v[8:9]
	v_ashrrev_i32_e32 v5, 31, v4
	v_lshl_add_u64 v[8:9], v[2:3], 0, v[8:9]
	v_lshlrev_b64 v[4:5], 13, v[4:5]
	v_lshl_add_u64 v[2:3], v[2:3], 0, v[4:5]
	global_load_dword v4, v[8:9], off nt
	global_load_dword v5, v[2:3], off nt
	v_add_u32_e32 v0, s23, v0
	v_mad_u64_u32 v[2:3], s[46:47], v7, s40, v[0:1]
	s_waitcnt vmcnt(31)
	v_mul_f32_e32 v8, 0x42800000, v25
	s_waitcnt vmcnt(30)
	v_mul_f32_e32 v3, 0x42800000, v26
	ds_write2_b32 v2, v8, v3 offset1:66
	s_waitcnt vmcnt(29)
	v_mul_f32_e32 v3, 0x42800000, v27
	s_waitcnt vmcnt(28)
	v_mul_f32_e32 v7, 0x42800000, v28
	ds_write2_b32 v2, v3, v7 offset0:132 offset1:198
	s_waitcnt vmcnt(27)
	v_mul_f32_e32 v3, 0x42800000, v29
	s_waitcnt vmcnt(26)
	v_mul_f32_e32 v7, 0x42800000, v30
	v_add_u32_e32 v8, 0x400, v2
	ds_write2_b32 v8, v3, v7 offset0:8 offset1:74
	s_waitcnt vmcnt(25)
	v_mul_f32_e32 v3, 0x42800000, v31
	s_waitcnt vmcnt(24)
	v_mul_f32_e32 v7, 0x42800000, v32
	ds_write2_b32 v8, v3, v7 offset0:140 offset1:206
	s_waitcnt vmcnt(23)
	v_mul_f32_e32 v3, 0x42800000, v33
	s_waitcnt vmcnt(22)
	v_mul_f32_e32 v7, 0x42800000, v34
	v_add_u32_e32 v8, 0x800, v2
	ds_write2_b32 v8, v3, v7 offset0:16 offset1:82
	s_waitcnt vmcnt(21)
	v_mul_f32_e32 v3, 0x42800000, v35
	s_waitcnt vmcnt(20)
	v_mul_f32_e32 v7, 0x42800000, v36
	ds_write2_b32 v8, v3, v7 offset0:148 offset1:214
	s_waitcnt vmcnt(19)
	v_mul_f32_e32 v3, 0x42800000, v37
	s_waitcnt vmcnt(18)
	v_mul_f32_e32 v7, 0x42800000, v38
	v_add_u32_e32 v8, 0xc00, v2
	ds_write2_b32 v8, v3, v7 offset0:24 offset1:90
	s_waitcnt vmcnt(17)
	v_mul_f32_e32 v3, 0x42800000, v39
	s_waitcnt vmcnt(16)
	v_mul_f32_e32 v7, 0x42800000, v40
	ds_write2_b32 v8, v3, v7 offset0:156 offset1:222
	v_add_u32_e32 v8, 0x1000, v2
	s_ashr_i32 s19, s18, 31
	s_waitcnt vmcnt(15)
	v_mul_f32_e32 v3, 0x42800000, v41
	s_waitcnt vmcnt(14)
	v_mul_f32_e32 v7, 0x42800000, v42
	ds_write2_b32 v8, v3, v7 offset0:32 offset1:98
	s_waitcnt vmcnt(13)
	v_mul_f32_e32 v3, 0x42800000, v43
	s_waitcnt vmcnt(12)
	v_mul_f32_e32 v7, 0x42800000, v44
	ds_write2_b32 v8, v3, v7 offset0:164 offset1:230
	s_waitcnt vmcnt(11)
	v_mul_f32_e32 v3, 0x42800000, v45
	s_waitcnt vmcnt(10)
	v_mul_f32_e32 v7, 0x42800000, v46
	v_add_u32_e32 v8, 0x1400, v2
	ds_write2_b32 v8, v3, v7 offset0:40 offset1:106
	s_waitcnt vmcnt(9)
	v_mul_f32_e32 v3, 0x42800000, v20
	s_waitcnt vmcnt(8)
	v_mul_f32_e32 v7, 0x42800000, v21
	ds_write2_b32 v8, v3, v7 offset0:172 offset1:238
	v_add_u32_e32 v8, 0x1800, v2
	v_add_u32_e32 v2, 0x1c00, v2
	s_waitcnt vmcnt(7)
	v_mul_f32_e32 v3, 0x42800000, v22
	s_waitcnt vmcnt(6)
	v_mul_f32_e32 v7, 0x42800000, v10
	ds_write2_b32 v8, v3, v7 offset0:48 offset1:114
	s_waitcnt vmcnt(5)
	v_mul_f32_e32 v3, 0x42800000, v11
	s_waitcnt vmcnt(4)
	v_mul_f32_e32 v7, 0x42800000, v12
	ds_write2_b32 v8, v3, v7 offset0:180 offset1:246
	s_waitcnt vmcnt(3)
	v_mul_f32_e32 v3, 0x42800000, v13
	s_waitcnt vmcnt(2)
	v_mul_f32_e32 v7, 0x42800000, v14
	ds_write2_b32 v2, v3, v7 offset0:56 offset1:122
	v_and_b32_e32 v10, 0xffffffe0, v6
	v_mad_u64_u32 v[8:9], s[46:47], v10, s40, v[0:1]
	s_waitcnt vmcnt(1)
	v_mul_f32_e32 v3, 0x42800000, v4
	s_waitcnt vmcnt(0)
	v_mul_f32_e32 v4, 0x42800000, v5
	ds_write2_b32 v2, v3, v4 offset0:188 offset1:254
	s_waitcnt lgkmcnt(0)
	ds_read2_b32 v[2:3], v8 offset1:33
	ds_read2_b32 v[4:5], v8 offset0:66 offset1:99
	ds_read2_b32 v[6:7], v8 offset0:132 offset1:165
	s_waitcnt lgkmcnt(2)
	v_med3_f32 v0, v2, s39, v162
	v_med3_f32 v3, v3, s39, v162
	v_mov_b32_e32 v2, v1
	v_cvt_pk_fp8_f32 v2, v0, v3
	s_waitcnt lgkmcnt(1)
	v_med3_f32 v0, v4, s39, v162
	v_med3_f32 v3, v5, s39, v162
	ds_read2_b32 v[4:5], v8 offset0:198 offset1:231
	v_cvt_pk_fp8_f32 v2, v0, v3 op_sel:[0,0,1]
	s_waitcnt lgkmcnt(1)
	v_med3_f32 v0, v6, s39, v162
	v_med3_f32 v6, v7, s39, v162
	v_mov_b32_e32 v3, v1
	v_cvt_pk_fp8_f32 v3, v0, v6
	v_add_u32_e32 v0, 0x400, v8
	ds_read2_b32 v[6:7], v0 offset0:8 offset1:41
	s_waitcnt lgkmcnt(1)
	v_med3_f32 v4, v4, s39, v162
	v_med3_f32 v5, v5, s39, v162
	v_cvt_pk_fp8_f32 v3, v4, v5 op_sel:[0,0,1]
	ds_read2_b32 v[12:13], v0 offset0:74 offset1:107
	s_waitcnt lgkmcnt(1)
	v_med3_f32 v5, v6, s39, v162
	v_med3_f32 v6, v7, s39, v162
	v_mov_b32_e32 v4, v1
	v_cvt_pk_fp8_f32 v4, v5, v6
	ds_read2_b32 v[6:7], v0 offset0:140 offset1:173
	s_waitcnt lgkmcnt(1)
	v_med3_f32 v5, v12, s39, v162
	v_med3_f32 v9, v13, s39, v162
	v_cvt_pk_fp8_f32 v4, v5, v9 op_sel:[0,0,1]
	ds_read2_b32 v[12:13], v0 offset0:206 offset1:239
	s_waitcnt lgkmcnt(1)
	v_med3_f32 v0, v6, s39, v162
	v_med3_f32 v6, v7, s39, v162
	v_mov_b32_e32 v5, v1
	v_cvt_pk_fp8_f32 v5, v0, v6
	v_add_u32_e32 v0, 0x800, v8
	ds_read2_b32 v[6:7], v0 offset0:16 offset1:49
	s_waitcnt lgkmcnt(1)
	v_med3_f32 v9, v12, s39, v162
	v_med3_f32 v11, v13, s39, v162
	ds_read2_b32 v[12:13], v0 offset0:82 offset1:115
	v_cvt_pk_fp8_f32 v5, v9, v11 op_sel:[0,0,1]
	s_waitcnt lgkmcnt(1)
	v_med3_f32 v9, v6, s39, v162
	v_med3_f32 v7, v7, s39, v162
	v_mov_b32_e32 v6, v1
	ds_read2_b32 v[14:15], v0 offset0:148 offset1:181
	v_cvt_pk_fp8_f32 v6, v9, v7
	s_waitcnt lgkmcnt(1)
	v_med3_f32 v7, v12, s39, v162
	v_med3_f32 v9, v13, s39, v162
	ds_read2_b32 v[12:13], v0 offset0:214 offset1:247
	v_cvt_pk_fp8_f32 v6, v7, v9 op_sel:[0,0,1]
	s_waitcnt lgkmcnt(1)
	v_med3_f32 v0, v14, s39, v162
	v_med3_f32 v9, v15, s39, v162
	v_mov_b32_e32 v7, v1
	v_cvt_pk_fp8_f32 v7, v0, v9
	v_add_u32_e32 v0, 0xc00, v8
	ds_read2_b32 v[8:9], v0 offset0:24 offset1:57
	s_waitcnt lgkmcnt(1)
	v_med3_f32 v11, v12, s39, v162
	ds_read2_b32 v[14:15], v0 offset0:90 offset1:123
	v_med3_f32 v12, v13, s39, v162
	v_cvt_pk_fp8_f32 v7, v11, v12 op_sel:[0,0,1]
	ds_read2_b32 v[12:13], v0 offset0:156 offset1:189
	s_waitcnt lgkmcnt(2)
	v_med3_f32 v11, v8, s39, v162
	v_med3_f32 v9, v9, s39, v162
	s_waitcnt lgkmcnt(1)
	v_med3_f32 v16, v14, s39, v162
	v_med3_f32 v17, v15, s39, v162
	v_mov_b32_e32 v8, v1
	ds_read2_b32 v[14:15], v0 offset0:222 offset1:255
	v_cvt_pk_fp8_f32 v8, v11, v9
	s_waitcnt lgkmcnt(1)
	v_med3_f32 v0, v12, s39, v162
	v_med3_f32 v11, v13, s39, v162
	v_mov_b32_e32 v9, v1
	v_cvt_pk_fp8_f32 v9, v0, v11
	v_or_b32_e32 v12, s20, v24
	v_ashrrev_i32_e32 v13, 31, v12
	s_waitcnt lgkmcnt(0)
	v_med3_f32 v0, v14, s39, v162
	v_med3_f32 v11, v15, s39, v162
	v_lshlrev_b64 v[12:13], 10, v[12:13]
	v_cvt_pk_fp8_f32 v8, v16, v17 op_sel:[0,0,1]
	v_cvt_pk_fp8_f32 v9, v0, v11 op_sel:[0,0,1]
	v_lshl_add_u64 v[12:13], s[2:3], 0, v[12:13]
	v_lshl_add_u64 v[12:13], v[12:13], 0, s[18:19]
	v_ashrrev_i32_e32 v11, 31, v10
	v_lshl_add_u64 v[10:11], v[12:13], 0, v[10:11]
	global_store_dwordx4 v[10:11], v[2:5], off
	global_store_dwordx4 v[10:11], v[6:9], off offset:16
	s_waitcnt lgkmcnt(0)
	s_branch .LBB0_1472

.LBB0_1481:
	s_cmpk_gt_i32 s15, 0x7fff
	s_mov_b64 s[2:3], -1
	s_cbranch_scc0 .LBB0_1483
	s_add_i32 s0, s15, 0xffff8000
	s_lshr_b32 s0, s0, 9
	s_lshl_b64 s[2:3], s[0:1], 20
	s_lshl_b64 s[4:5], s[0:1], 22
	s_add_u32 s6, s12, s4
	s_addc_u32 s5, s13, s5
	s_add_u32 s2, s14, s2
	s_addc_u32 s3, s16, s3
	s_and_b32 s4, s21, 0x3e0
	s_and_b32 s0, s19, 0x3c0
	s_lshl_b32 s7, s4, 2
	s_add_u32 s6, s6, s7
	v_add_u32_e32 v54, s0, v1
	s_addc_u32 s7, s5, 0
	v_ashrrev_i32_e32 v55, 31, v54
	v_add_u32_e32 v56, s0, v10
	v_add_u32_e32 v58, s0, v11
	v_add_u32_e32 v60, s0, v12
	v_add_u32_e32 v62, s0, v13
	v_add_u32_e32 v64, s0, v14
	v_add_u32_e32 v66, s0, v15
	v_add_u32_e32 v68, s0, v16
	v_lshl_add_u64 v[8:9], s[6:7], 0, v[2:3]
	v_lshlrev_b64 v[54:55], 12, v[54:55]
	v_ashrrev_i32_e32 v57, 31, v56
	v_ashrrev_i32_e32 v59, 31, v58
	v_ashrrev_i32_e32 v61, 31, v60
	v_ashrrev_i32_e32 v63, 31, v62
	v_ashrrev_i32_e32 v65, 31, v64
	v_ashrrev_i32_e32 v67, 31, v66
	v_ashrrev_i32_e32 v69, 31, v68
	v_lshl_add_u64 v[54:55], v[8:9], 0, v[54:55]
	v_lshlrev_b64 v[56:57], 12, v[56:57]
	v_lshlrev_b64 v[58:59], 12, v[58:59]
	v_lshlrev_b64 v[60:61], 12, v[60:61]
	v_lshlrev_b64 v[62:63], 12, v[62:63]
	v_lshlrev_b64 v[64:65], 12, v[64:65]
	v_lshlrev_b64 v[66:67], 12, v[66:67]
	v_lshlrev_b64 v[68:69], 12, v[68:69]
	v_lshl_add_u64 v[56:57], v[8:9], 0, v[56:57]
	v_lshl_add_u64 v[58:59], v[8:9], 0, v[58:59]
	v_lshl_add_u64 v[60:61], v[8:9], 0, v[60:61]
	v_lshl_add_u64 v[62:63], v[8:9], 0, v[62:63]
	v_lshl_add_u64 v[64:65], v[8:9], 0, v[64:65]
	v_lshl_add_u64 v[66:67], v[8:9], 0, v[66:67]
	v_lshl_add_u64 v[68:69], v[8:9], 0, v[68:69]
	global_load_dword v53, v[54:55], off nt
	global_load_dword v70, v[56:57], off nt
	global_load_dword v71, v[58:59], off nt
	global_load_dword v72, v[60:61], off nt
	global_load_dword v73, v[62:63], off nt
	global_load_dword v74, v[64:65], off nt
	global_load_dword v75, v[66:67], off nt
	global_load_dword v76, v[68:69], off nt
	v_add_u32_e32 v54, s0, v17
	v_ashrrev_i32_e32 v55, 31, v54
	v_add_u32_e32 v56, s0, v18
	v_add_u32_e32 v58, s0, v19
	v_add_u32_e32 v60, s0, v20
	v_add_u32_e32 v62, s0, v21
	v_add_u32_e32 v64, s0, v22
	v_add_u32_e32 v66, s0, v23
	v_add_u32_e32 v68, s0, v24
	v_lshlrev_b64 v[54:55], 12, v[54:55]
	v_ashrrev_i32_e32 v57, 31, v56
	v_ashrrev_i32_e32 v59, 31, v58
	v_ashrrev_i32_e32 v61, 31, v60
	v_ashrrev_i32_e32 v63, 31, v62
	v_ashrrev_i32_e32 v65, 31, v64
	v_ashrrev_i32_e32 v67, 31, v66
	v_ashrrev_i32_e32 v69, 31, v68
	v_lshl_add_u64 v[54:55], v[8:9], 0, v[54:55]
	v_lshlrev_b64 v[56:57], 12, v[56:57]
	v_lshlrev_b64 v[58:59], 12, v[58:59]
	v_lshlrev_b64 v[60:61], 12, v[60:61]
	v_lshlrev_b64 v[62:63], 12, v[62:63]
	v_lshlrev_b64 v[64:65], 12, v[64:65]
	v_lshlrev_b64 v[66:67], 12, v[66:67]
	v_lshlrev_b64 v[68:69], 12, v[68:69]
	v_lshl_add_u64 v[56:57], v[8:9], 0, v[56:57]
	v_lshl_add_u64 v[58:59], v[8:9], 0, v[58:59]
	v_lshl_add_u64 v[60:61], v[8:9], 0, v[60:61]
	v_lshl_add_u64 v[62:63], v[8:9], 0, v[62:63]
	v_lshl_add_u64 v[64:65], v[8:9], 0, v[64:65]
	v_lshl_add_u64 v[66:67], v[8:9], 0, v[66:67]
	v_lshl_add_u64 v[68:69], v[8:9], 0, v[68:69]
	global_load_dword v77, v[54:55], off nt
	global_load_dword v78, v[56:57], off nt
	global_load_dword v79, v[58:59], off nt
	global_load_dword v80, v[60:61], off nt
	global_load_dword v81, v[62:63], off nt
	global_load_dword v82, v[64:65], off nt
	global_load_dword v83, v[66:67], off nt
	global_load_dword v84, v[68:69], off nt
	v_add_u32_e32 v54, s0, v25
	v_ashrrev_i32_e32 v55, 31, v54
	v_add_u32_e32 v56, s0, v26
	v_add_u32_e32 v58, s0, v27
	v_add_u32_e32 v60, s0, v28
	v_add_u32_e32 v62, s0, v29
	v_add_u32_e32 v64, s0, v30
	v_add_u32_e32 v66, s0, v31
	v_add_u32_e32 v68, s0, v32
	v_lshlrev_b64 v[54:55], 12, v[54:55]
	v_ashrrev_i32_e32 v57, 31, v56
	v_ashrrev_i32_e32 v59, 31, v58
	v_ashrrev_i32_e32 v61, 31, v60
	v_ashrrev_i32_e32 v63, 31, v62
	v_ashrrev_i32_e32 v65, 31, v64
	v_ashrrev_i32_e32 v67, 31, v66
	v_ashrrev_i32_e32 v69, 31, v68
	v_lshl_add_u64 v[54:55], v[8:9], 0, v[54:55]
	v_lshlrev_b64 v[56:57], 12, v[56:57]
	v_lshlrev_b64 v[58:59], 12, v[58:59]
	v_lshlrev_b64 v[60:61], 12, v[60:61]
	v_lshlrev_b64 v[62:63], 12, v[62:63]
	v_lshlrev_b64 v[64:65], 12, v[64:65]
	v_lshlrev_b64 v[66:67], 12, v[66:67]
	v_lshlrev_b64 v[68:69], 12, v[68:69]
	v_lshl_add_u64 v[56:57], v[8:9], 0, v[56:57]
	v_lshl_add_u64 v[58:59], v[8:9], 0, v[58:59]
	v_lshl_add_u64 v[60:61], v[8:9], 0, v[60:61]
	v_lshl_add_u64 v[62:63], v[8:9], 0, v[62:63]
	v_lshl_add_u64 v[64:65], v[8:9], 0, v[64:65]
	v_lshl_add_u64 v[66:67], v[8:9], 0, v[66:67]
	v_lshl_add_u64 v[68:69], v[8:9], 0, v[68:69]
	global_load_dword v85, v[54:55], off nt
	global_load_dword v86, v[56:57], off nt
	global_load_dword v87, v[58:59], off nt
	global_load_dword v88, v[60:61], off nt
	global_load_dword v89, v[62:63], off nt
	global_load_dword v90, v[64:65], off nt
	global_load_dword v91, v[66:67], off nt
	global_load_dword v92, v[68:69], off nt
	v_add_u32_e32 v54, s0, v33
	v_ashrrev_i32_e32 v55, 31, v54
	v_add_u32_e32 v56, s0, v34
	v_add_u32_e32 v58, s0, v35
	v_add_u32_e32 v60, s0, v36
	v_add_u32_e32 v62, s0, v37
	v_add_u32_e32 v64, s0, v38
	v_lshlrev_b64 v[54:55], 12, v[54:55]
	v_ashrrev_i32_e32 v57, 31, v56
	v_ashrrev_i32_e32 v59, 31, v58
	v_ashrrev_i32_e32 v61, 31, v60
	v_ashrrev_i32_e32 v63, 31, v62
	v_ashrrev_i32_e32 v65, 31, v64
	v_lshl_add_u64 v[54:55], v[8:9], 0, v[54:55]
	v_lshlrev_b64 v[56:57], 12, v[56:57]
	v_lshlrev_b64 v[58:59], 12, v[58:59]
	v_lshlrev_b64 v[60:61], 12, v[60:61]
	v_lshlrev_b64 v[62:63], 12, v[62:63]
	v_lshlrev_b64 v[64:65], 12, v[64:65]
	v_lshl_add_u64 v[56:57], v[8:9], 0, v[56:57]
	v_lshl_add_u64 v[58:59], v[8:9], 0, v[58:59]
	v_lshl_add_u64 v[60:61], v[8:9], 0, v[60:61]
	v_lshl_add_u64 v[62:63], v[8:9], 0, v[62:63]
	v_lshl_add_u64 v[64:65], v[8:9], 0, v[64:65]
	global_load_dword v66, v[54:55], off nt
	global_load_dword v67, v[56:57], off nt
	global_load_dword v68, v[58:59], off nt
	global_load_dword v69, v[60:61], off nt
	global_load_dword v93, v[62:63], off nt
	global_load_dword v94, v[64:65], off nt
	v_add_u32_e32 v54, s0, v39
	v_ashrrev_i32_e32 v55, 31, v54
	v_add_u32_e32 v56, s0, v40
	v_lshlrev_b64 v[54:55], 12, v[54:55]
	v_ashrrev_i32_e32 v57, 31, v56
	v_lshl_add_u64 v[54:55], v[8:9], 0, v[54:55]
	v_lshlrev_b64 v[56:57], 12, v[56:57]
	v_lshl_add_u64 v[8:9], v[8:9], 0, v[56:57]
	global_load_dword v56, v[54:55], off nt
	global_load_dword v57, v[8:9], off nt
	s_waitcnt vmcnt(31)
	v_mul_f32_e32 v8, 0x42800000, v53
	s_waitcnt vmcnt(30)
	v_mul_f32_e32 v9, 0x42800000, v70
	ds_write2_b32 v7, v8, v9 offset1:66
	s_waitcnt vmcnt(29)
	v_mul_f32_e32 v8, 0x42800000, v71
	s_waitcnt vmcnt(28)
	v_mul_f32_e32 v9, 0x42800000, v72
	ds_write2_b32 v7, v8, v9 offset0:132 offset1:198
	s_waitcnt vmcnt(27)
	v_mul_f32_e32 v8, 0x42800000, v73
	s_waitcnt vmcnt(26)
	v_mul_f32_e32 v9, 0x42800000, v74
	ds_write2_b32 v43, v8, v9 offset0:8 offset1:74
	s_waitcnt vmcnt(25)
	v_mul_f32_e32 v8, 0x42800000, v75
	s_waitcnt vmcnt(24)
	v_mul_f32_e32 v9, 0x42800000, v76
	ds_write2_b32 v41, v8, v9 offset1:66
	s_waitcnt vmcnt(23)
	v_mul_f32_e32 v8, 0x42800000, v77
	s_waitcnt vmcnt(22)
	v_mul_f32_e32 v9, 0x42800000, v78
	ds_write2_b32 v41, v8, v9 offset0:132 offset1:198
	s_waitcnt vmcnt(21)
	v_mul_f32_e32 v8, 0x42800000, v79
	s_waitcnt vmcnt(20)
	v_mul_f32_e32 v9, 0x42800000, v80
	ds_write2_b32 v44, v8, v9 offset0:8 offset1:74
	s_waitcnt vmcnt(19)
	v_mul_f32_e32 v8, 0x42800000, v81
	s_waitcnt vmcnt(18)
	v_mul_f32_e32 v9, 0x42800000, v82
	ds_write2_b32 v42, v8, v9 offset1:66
	s_waitcnt vmcnt(17)
	v_mul_f32_e32 v8, 0x42800000, v83
	s_waitcnt vmcnt(16)
	v_mul_f32_e32 v9, 0x42800000, v84
	ds_write2_b32 v42, v8, v9 offset0:132 offset1:198
	v_mov_b32_e32 v54, v3
	s_waitcnt vmcnt(15)
	v_mul_f32_e32 v8, 0x42800000, v85
	s_waitcnt vmcnt(14)
	v_mul_f32_e32 v9, 0x42800000, v86
	ds_write2_b32 v45, v8, v9 offset0:8 offset1:74
	s_waitcnt vmcnt(13)
	v_mul_f32_e32 v8, 0x42800000, v87
	s_waitcnt vmcnt(12)
	v_mul_f32_e32 v9, 0x42800000, v88
	ds_write2_b32 v45, v8, v9 offset0:140 offset1:206
	s_waitcnt vmcnt(11)
	v_mul_f32_e32 v8, 0x42800000, v89
	s_waitcnt vmcnt(10)
	v_mul_f32_e32 v9, 0x42800000, v90
	ds_write2_b32 v46, v8, v9 offset0:16 offset1:82
	s_waitcnt vmcnt(9)
	v_mul_f32_e32 v8, 0x42800000, v91
	s_waitcnt vmcnt(8)
	v_mul_f32_e32 v9, 0x42800000, v92
	ds_write2_b32 v46, v8, v9 offset0:148 offset1:214
	s_waitcnt vmcnt(7)
	v_mul_f32_e32 v8, 0x42800000, v66
	s_waitcnt vmcnt(6)
	v_mul_f32_e32 v9, 0x42800000, v67
	ds_write2_b32 v47, v8, v9 offset0:24 offset1:90
	s_waitcnt vmcnt(5)
	v_mul_f32_e32 v8, 0x42800000, v68
	s_waitcnt vmcnt(4)
	v_mul_f32_e32 v9, 0x42800000, v69
	ds_write2_b32 v47, v8, v9 offset0:156 offset1:222
	s_waitcnt vmcnt(3)
	v_mul_f32_e32 v8, 0x42800000, v93
	s_waitcnt vmcnt(2)
	v_mul_f32_e32 v9, 0x42800000, v94
	ds_write2_b32 v48, v8, v9 offset0:32 offset1:98
	s_waitcnt vmcnt(1)
	v_mul_f32_e32 v8, 0x42800000, v56
	s_waitcnt vmcnt(0)
	v_mul_f32_e32 v9, 0x42800000, v57
	ds_write2_b32 v48, v8, v9 offset0:164 offset1:230
	s_waitcnt lgkmcnt(0)
	ds_read2_b32 v[8:9], v6 offset1:33
	ds_read2_b32 v[56:57], v6 offset0:66 offset1:99
	ds_read2_b32 v[58:59], v50 offset0:74 offset1:107
	ds_read2_b32 v[60:61], v51 offset0:82 offset1:115
	ds_read2_b32 v[62:63], v52 offset0:90 offset1:123
	s_waitcnt lgkmcnt(4)
	v_med3_f32 v8, v8, s24, v49
	v_med3_f32 v9, v9, s24, v49
	v_cvt_pk_fp8_f32 v54, v8, v9
	ds_read2_b32 v[8:9], v6 offset0:132 offset1:165
	s_waitcnt lgkmcnt(4)
	v_med3_f32 v53, v56, s24, v49
	v_med3_f32 v55, v57, s24, v49
	v_cvt_pk_fp8_f32 v54, v53, v55 op_sel:[0,0,1]
	ds_read2_b32 v[56:57], v6 offset0:198 offset1:231
	s_waitcnt lgkmcnt(1)
	v_med3_f32 v8, v8, s24, v49
	v_med3_f32 v9, v9, s24, v49
	v_mov_b32_e32 v55, v3
	v_cvt_pk_fp8_f32 v55, v8, v9
	ds_read2_b32 v[8:9], v50 offset0:8 offset1:41
	s_waitcnt lgkmcnt(1)
	v_med3_f32 v53, v56, s24, v49
	v_med3_f32 v56, v57, s24, v49
	v_cvt_pk_fp8_f32 v55, v53, v56 op_sel:[0,0,1]
	v_mov_b32_e32 v56, v3
	s_waitcnt lgkmcnt(0)
	v_med3_f32 v8, v8, s24, v49
	v_med3_f32 v9, v9, s24, v49
	v_cvt_pk_fp8_f32 v56, v8, v9
	ds_read2_b32 v[8:9], v50 offset0:140 offset1:173
	v_med3_f32 v53, v58, s24, v49
	v_med3_f32 v57, v59, s24, v49
	v_cvt_pk_fp8_f32 v56, v53, v57 op_sel:[0,0,1]
	ds_read2_b32 v[58:59], v50 offset0:206 offset1:239
	s_waitcnt lgkmcnt(1)
	v_med3_f32 v8, v8, s24, v49
	v_med3_f32 v9, v9, s24, v49
	v_mov_b32_e32 v57, v3
	v_cvt_pk_fp8_f32 v57, v8, v9
	ds_read2_b32 v[8:9], v51 offset0:16 offset1:49
	s_waitcnt lgkmcnt(1)
	v_med3_f32 v53, v58, s24, v49
	v_med3_f32 v58, v59, s24, v49
	v_cvt_pk_fp8_f32 v57, v53, v58 op_sel:[0,0,1]
	v_mov_b32_e32 v58, v3
	s_waitcnt lgkmcnt(0)
	v_med3_f32 v8, v8, s24, v49
	v_med3_f32 v9, v9, s24, v49
	v_cvt_pk_fp8_f32 v58, v8, v9
	ds_read2_b32 v[8:9], v51 offset0:148 offset1:181
	v_med3_f32 v53, v60, s24, v49
	v_med3_f32 v59, v61, s24, v49
	v_cvt_pk_fp8_f32 v58, v53, v59 op_sel:[0,0,1]
	ds_read2_b32 v[60:61], v51 offset0:214 offset1:247
	s_waitcnt lgkmcnt(1)
	v_med3_f32 v8, v8, s24, v49
	v_med3_f32 v9, v9, s24, v49
	v_mov_b32_e32 v59, v3
	v_cvt_pk_fp8_f32 v59, v8, v9
	ds_read2_b32 v[8:9], v52 offset0:24 offset1:57
	s_waitcnt lgkmcnt(1)
	v_med3_f32 v53, v60, s24, v49
	v_med3_f32 v60, v61, s24, v49
	v_cvt_pk_fp8_f32 v59, v53, v60 op_sel:[0,0,1]
	v_med3_f32 v64, v62, s24, v49
	s_waitcnt lgkmcnt(0)
	v_med3_f32 v53, v8, s24, v49
	v_med3_f32 v61, v9, s24, v49
	ds_read2_b32 v[8:9], v52 offset0:156 offset1:189
	v_med3_f32 v65, v63, s24, v49
	v_mov_b32_e32 v60, v3
	ds_read2_b32 v[62:63], v52 offset0:222 offset1:255
	v_cvt_pk_fp8_f32 v60, v53, v61
	s_waitcnt lgkmcnt(1)
	v_med3_f32 v8, v8, s24, v49
	v_med3_f32 v9, v9, s24, v49
	v_mov_b32_e32 v61, v3
	v_cvt_pk_fp8_f32 v61, v8, v9
	s_waitcnt lgkmcnt(0)
	v_med3_f32 v8, v62, s24, v49
	v_med3_f32 v9, v63, s24, v49
	v_cvt_pk_fp8_f32 v60, v64, v65 op_sel:[0,0,1]
	v_cvt_pk_fp8_f32 v61, v8, v9 op_sel:[0,0,1]
	v_or_b32_e32 v8, s4, v0
	v_lshlrev_b32_e32 v8, 10, v8
	v_mov_b32_e32 v9, v3
	v_lshl_add_u64 v[8:9], s[2:3], 0, v[8:9]
	v_lshl_add_u64 v[8:9], v[8:9], 0, s[0:1]
	v_lshl_add_u64 v[8:9], v[8:9], 0, v[4:5]
	global_store_dwordx4 v[8:9], v[54:57], off
	global_store_dwordx4 v[8:9], v[58:61], off offset:16
	s_waitcnt lgkmcnt(0)
	s_mov_b64 s[2:3], 0
.LBB0_1483:
	s_andn2_b64 vcc, exec, s[2:3]
	s_cbranch_vccnz .LBB0_1480
	s_ashr_i32 s0, s15, 31
	s_lshr_b32 s0, s0, 22
	s_add_i32 s0, s15, s0
	s_ashr_i32 s2, s0, 10
	s_and_b32 s0, s0, 0xfc00
	s_ashr_i32 s3, s2, 31
	s_sub_i32 s0, s15, s0
	s_lshl_b64 s[4:5], s[2:3], 23
	s_add_u32 s25, s10, s4
	s_addc_u32 s5, s11, s5
	s_lshl_b64 s[2:3], s[2:3], 21
	s_add_u32 s2, s17, s2
	s_sext_i32_i16 s4, s0
	s_addc_u32 s3, s18, s3
	s_bfe_u32 s4, s4, 0x60019
	s_add_i32 s4, s0, s4
	s_sext_i32_i16 s6, s4
	s_and_b32 s4, s4, 0xffc0
	s_sub_i32 s0, s0, s4
	s_sext_i32_i16 s0, s0
	s_and_b32 s4, s6, 0xffffffc0
	s_lshl_b32 s6, s0, 5
	s_ashr_i32 s7, s6, 31
	s_lshl_b64 s[26:27], s[6:7], 2
	s_add_u32 s26, s25, s26
	v_add_u32_e32 v54, s4, v1
	s_addc_u32 s27, s5, s27
	v_ashrrev_i32_e32 v55, 31, v54
	v_add_u32_e32 v56, s4, v10
	v_add_u32_e32 v58, s4, v11
	v_add_u32_e32 v60, s4, v12
	v_add_u32_e32 v62, s4, v13
	v_add_u32_e32 v64, s4, v14
	v_add_u32_e32 v66, s4, v15
	v_add_u32_e32 v68, s4, v16
	v_lshl_add_u64 v[8:9], s[26:27], 0, v[2:3]
	v_lshlrev_b64 v[54:55], 13, v[54:55]
	v_ashrrev_i32_e32 v57, 31, v56
	v_ashrrev_i32_e32 v59, 31, v58
	v_ashrrev_i32_e32 v61, 31, v60
	v_ashrrev_i32_e32 v63, 31, v62
	v_ashrrev_i32_e32 v65, 31, v64
	v_ashrrev_i32_e32 v67, 31, v66
	v_ashrrev_i32_e32 v69, 31, v68
	v_lshl_add_u64 v[54:55], v[8:9], 0, v[54:55]
	v_lshlrev_b64 v[56:57], 13, v[56:57]
	v_lshlrev_b64 v[58:59], 13, v[58:59]
	v_lshlrev_b64 v[60:61], 13, v[60:61]
	v_lshlrev_b64 v[62:63], 13, v[62:63]
	v_lshlrev_b64 v[64:65], 13, v[64:65]
	v_lshlrev_b64 v[66:67], 13, v[66:67]
	v_lshlrev_b64 v[68:69], 13, v[68:69]
	v_lshl_add_u64 v[56:57], v[8:9], 0, v[56:57]
	v_lshl_add_u64 v[58:59], v[8:9], 0, v[58:59]
	v_lshl_add_u64 v[60:61], v[8:9], 0, v[60:61]
	v_lshl_add_u64 v[62:63], v[8:9], 0, v[62:63]
	v_lshl_add_u64 v[64:65], v[8:9], 0, v[64:65]
	v_lshl_add_u64 v[66:67], v[8:9], 0, v[66:67]
	v_lshl_add_u64 v[68:69], v[8:9], 0, v[68:69]
	global_load_dword v53, v[54:55], off nt
	global_load_dword v70, v[56:57], off nt
	global_load_dword v71, v[58:59], off nt
	global_load_dword v72, v[60:61], off nt
	global_load_dword v73, v[62:63], off nt
	global_load_dword v74, v[64:65], off nt
	global_load_dword v75, v[66:67], off nt
	global_load_dword v76, v[68:69], off nt
	v_add_u32_e32 v54, s4, v17
	v_ashrrev_i32_e32 v55, 31, v54
	v_add_u32_e32 v56, s4, v18
	v_add_u32_e32 v58, s4, v19
	v_add_u32_e32 v60, s4, v20
	v_add_u32_e32 v62, s4, v21
	v_add_u32_e32 v64, s4, v22
	v_add_u32_e32 v66, s4, v23
	v_add_u32_e32 v68, s4, v24
	v_lshlrev_b64 v[54:55], 13, v[54:55]
	v_ashrrev_i32_e32 v57, 31, v56
	v_ashrrev_i32_e32 v59, 31, v58
	v_ashrrev_i32_e32 v61, 31, v60
	v_ashrrev_i32_e32 v63, 31, v62
	v_ashrrev_i32_e32 v65, 31, v64
	v_ashrrev_i32_e32 v67, 31, v66
	v_ashrrev_i32_e32 v69, 31, v68
	v_lshl_add_u64 v[54:55], v[8:9], 0, v[54:55]
	v_lshlrev_b64 v[56:57], 13, v[56:57]
	v_lshlrev_b64 v[58:59], 13, v[58:59]
	v_lshlrev_b64 v[60:61], 13, v[60:61]
	v_lshlrev_b64 v[62:63], 13, v[62:63]
	v_lshlrev_b64 v[64:65], 13, v[64:65]
	v_lshlrev_b64 v[66:67], 13, v[66:67]
	v_lshlrev_b64 v[68:69], 13, v[68:69]
	v_lshl_add_u64 v[56:57], v[8:9], 0, v[56:57]
	v_lshl_add_u64 v[58:59], v[8:9], 0, v[58:59]
	v_lshl_add_u64 v[60:61], v[8:9], 0, v[60:61]
	v_lshl_add_u64 v[62:63], v[8:9], 0, v[62:63]
	v_lshl_add_u64 v[64:65], v[8:9], 0, v[64:65]
	v_lshl_add_u64 v[66:67], v[8:9], 0, v[66:67]
	v_lshl_add_u64 v[68:69], v[8:9], 0, v[68:69]
	global_load_dword v77, v[54:55], off nt
	global_load_dword v78, v[56:57], off nt
	global_load_dword v79, v[58:59], off nt
	global_load_dword v80, v[60:61], off nt
	global_load_dword v81, v[62:63], off nt
	global_load_dword v82, v[64:65], off nt
	global_load_dword v83, v[66:67], off nt
	global_load_dword v84, v[68:69], off nt
	v_add_u32_e32 v54, s4, v25
	v_ashrrev_i32_e32 v55, 31, v54
	v_add_u32_e32 v56, s4, v26
	v_add_u32_e32 v58, s4, v27
	v_add_u32_e32 v60, s4, v28
	v_add_u32_e32 v62, s4, v29
	v_add_u32_e32 v64, s4, v30
	v_add_u32_e32 v66, s4, v31
	v_add_u32_e32 v68, s4, v32
	v_lshlrev_b64 v[54:55], 13, v[54:55]
	v_ashrrev_i32_e32 v57, 31, v56
	v_ashrrev_i32_e32 v59, 31, v58
	v_ashrrev_i32_e32 v61, 31, v60
	v_ashrrev_i32_e32 v63, 31, v62
	v_ashrrev_i32_e32 v65, 31, v64
	v_ashrrev_i32_e32 v67, 31, v66
	v_ashrrev_i32_e32 v69, 31, v68
	v_lshl_add_u64 v[54:55], v[8:9], 0, v[54:55]
	v_lshlrev_b64 v[56:57], 13, v[56:57]
	v_lshlrev_b64 v[58:59], 13, v[58:59]
	v_lshlrev_b64 v[60:61], 13, v[60:61]
	v_lshlrev_b64 v[62:63], 13, v[62:63]
	v_lshlrev_b64 v[64:65], 13, v[64:65]
	v_lshlrev_b64 v[66:67], 13, v[66:67]
	v_lshlrev_b64 v[68:69], 13, v[68:69]
	v_lshl_add_u64 v[56:57], v[8:9], 0, v[56:57]
	v_lshl_add_u64 v[58:59], v[8:9], 0, v[58:59]
	v_lshl_add_u64 v[60:61], v[8:9], 0, v[60:61]
	v_lshl_add_u64 v[62:63], v[8:9], 0, v[62:63]
	v_lshl_add_u64 v[64:65], v[8:9], 0, v[64:65]
	v_lshl_add_u64 v[66:67], v[8:9], 0, v[66:67]
	v_lshl_add_u64 v[68:69], v[8:9], 0, v[68:69]
	global_load_dword v85, v[54:55], off nt
	global_load_dword v86, v[56:57], off nt
	global_load_dword v87, v[58:59], off nt
	global_load_dword v88, v[60:61], off nt
	global_load_dword v89, v[62:63], off nt
	global_load_dword v90, v[64:65], off nt
	global_load_dword v91, v[66:67], off nt
	global_load_dword v92, v[68:69], off nt
	v_add_u32_e32 v54, s4, v33
	v_ashrrev_i32_e32 v55, 31, v54
	v_add_u32_e32 v56, s4, v34
	v_add_u32_e32 v58, s4, v35
	v_add_u32_e32 v60, s4, v36
	v_add_u32_e32 v62, s4, v37
	v_add_u32_e32 v64, s4, v38
	v_lshlrev_b64 v[54:55], 13, v[54:55]
	v_ashrrev_i32_e32 v57, 31, v56
	v_ashrrev_i32_e32 v59, 31, v58
	v_ashrrev_i32_e32 v61, 31, v60
	v_ashrrev_i32_e32 v63, 31, v62
	v_ashrrev_i32_e32 v65, 31, v64
	v_lshl_add_u64 v[54:55], v[8:9], 0, v[54:55]
	v_lshlrev_b64 v[56:57], 13, v[56:57]
	v_lshlrev_b64 v[58:59], 13, v[58:59]
	v_lshlrev_b64 v[60:61], 13, v[60:61]
	v_lshlrev_b64 v[62:63], 13, v[62:63]
	v_lshlrev_b64 v[64:65], 13, v[64:65]
	v_lshl_add_u64 v[56:57], v[8:9], 0, v[56:57]
	v_lshl_add_u64 v[58:59], v[8:9], 0, v[58:59]
	v_lshl_add_u64 v[60:61], v[8:9], 0, v[60:61]
	v_lshl_add_u64 v[62:63], v[8:9], 0, v[62:63]
	v_lshl_add_u64 v[64:65], v[8:9], 0, v[64:65]
	global_load_dword v66, v[54:55], off nt
	global_load_dword v67, v[56:57], off nt
	global_load_dword v68, v[58:59], off nt
	global_load_dword v69, v[60:61], off nt
	global_load_dword v93, v[62:63], off nt
	global_load_dword v94, v[64:65], off nt
	v_add_u32_e32 v54, s4, v39
	v_ashrrev_i32_e32 v55, 31, v54
	v_add_u32_e32 v56, s4, v40
	v_lshlrev_b64 v[54:55], 13, v[54:55]
	v_ashrrev_i32_e32 v57, 31, v56
	v_lshl_add_u64 v[54:55], v[8:9], 0, v[54:55]
	v_lshlrev_b64 v[56:57], 13, v[56:57]
	v_lshl_add_u64 v[8:9], v[8:9], 0, v[56:57]
	global_load_dword v56, v[54:55], off nt
	global_load_dword v57, v[8:9], off nt
	s_waitcnt vmcnt(31)
	v_mul_f32_e32 v8, 0x42800000, v53
	s_waitcnt vmcnt(30)
	v_mul_f32_e32 v9, 0x42800000, v70
	ds_write2_b32 v7, v8, v9 offset1:66
	s_waitcnt vmcnt(29)
	v_mul_f32_e32 v8, 0x42800000, v71
	s_waitcnt vmcnt(28)
	v_mul_f32_e32 v9, 0x42800000, v72
	ds_write2_b32 v7, v8, v9 offset0:132 offset1:198
	s_waitcnt vmcnt(27)
	v_mul_f32_e32 v8, 0x42800000, v73
	s_waitcnt vmcnt(26)
	v_mul_f32_e32 v9, 0x42800000, v74
	ds_write2_b32 v43, v8, v9 offset0:8 offset1:74
	s_waitcnt vmcnt(25)
	v_mul_f32_e32 v8, 0x42800000, v75
	s_waitcnt vmcnt(24)
	v_mul_f32_e32 v9, 0x42800000, v76
	ds_write2_b32 v41, v8, v9 offset1:66
	s_waitcnt vmcnt(23)
	v_mul_f32_e32 v8, 0x42800000, v77
	s_waitcnt vmcnt(22)
	v_mul_f32_e32 v9, 0x42800000, v78
	ds_write2_b32 v41, v8, v9 offset0:132 offset1:198
	s_waitcnt vmcnt(21)
	v_mul_f32_e32 v8, 0x42800000, v79
	s_waitcnt vmcnt(20)
	v_mul_f32_e32 v9, 0x42800000, v80
	ds_write2_b32 v44, v8, v9 offset0:8 offset1:74
	s_waitcnt vmcnt(19)
	v_mul_f32_e32 v8, 0x42800000, v81
	s_waitcnt vmcnt(18)
	v_mul_f32_e32 v9, 0x42800000, v82
	ds_write2_b32 v42, v8, v9 offset1:66
	s_waitcnt vmcnt(17)
	v_mul_f32_e32 v8, 0x42800000, v83
	s_waitcnt vmcnt(16)
	v_mul_f32_e32 v9, 0x42800000, v84
	ds_write2_b32 v42, v8, v9 offset0:132 offset1:198
	v_mov_b32_e32 v54, v3
	s_ashr_i32 s5, s4, 31
	s_waitcnt vmcnt(15)
	v_mul_f32_e32 v8, 0x42800000, v85
	s_waitcnt vmcnt(14)
	v_mul_f32_e32 v9, 0x42800000, v86
	ds_write2_b32 v45, v8, v9 offset0:8 offset1:74
	s_waitcnt vmcnt(13)
	v_mul_f32_e32 v8, 0x42800000, v87
	s_waitcnt vmcnt(12)
	v_mul_f32_e32 v9, 0x42800000, v88
	ds_write2_b32 v45, v8, v9 offset0:140 offset1:206
	s_waitcnt vmcnt(11)
	v_mul_f32_e32 v8, 0x42800000, v89
	s_waitcnt vmcnt(10)
	v_mul_f32_e32 v9, 0x42800000, v90
	ds_write2_b32 v46, v8, v9 offset0:16 offset1:82
	s_waitcnt vmcnt(9)
	v_mul_f32_e32 v8, 0x42800000, v91
	s_waitcnt vmcnt(8)
	v_mul_f32_e32 v9, 0x42800000, v92
	ds_write2_b32 v46, v8, v9 offset0:148 offset1:214
	s_waitcnt vmcnt(7)
	v_mul_f32_e32 v8, 0x42800000, v66
	s_waitcnt vmcnt(6)
	v_mul_f32_e32 v9, 0x42800000, v67
	ds_write2_b32 v47, v8, v9 offset0:24 offset1:90
	s_waitcnt vmcnt(5)
	v_mul_f32_e32 v8, 0x42800000, v68
	s_waitcnt vmcnt(4)
	v_mul_f32_e32 v9, 0x42800000, v69
	ds_write2_b32 v47, v8, v9 offset0:156 offset1:222
	s_waitcnt vmcnt(3)
	v_mul_f32_e32 v8, 0x42800000, v93
	s_waitcnt vmcnt(2)
	v_mul_f32_e32 v9, 0x42800000, v94
	ds_write2_b32 v48, v8, v9 offset0:32 offset1:98
	s_waitcnt vmcnt(1)
	v_mul_f32_e32 v8, 0x42800000, v56
	s_waitcnt vmcnt(0)
	v_mul_f32_e32 v9, 0x42800000, v57
	ds_write2_b32 v48, v8, v9 offset0:164 offset1:230
	s_waitcnt lgkmcnt(0)
	ds_read2_b32 v[8:9], v6 offset1:33
	ds_read2_b32 v[56:57], v6 offset0:66 offset1:99
	ds_read2_b32 v[58:59], v50 offset0:74 offset1:107
	ds_read2_b32 v[60:61], v51 offset0:82 offset1:115
	ds_read2_b32 v[62:63], v52 offset0:90 offset1:123
	s_waitcnt lgkmcnt(4)
	v_med3_f32 v8, v8, s24, v49
	v_med3_f32 v9, v9, s24, v49
	v_cvt_pk_fp8_f32 v54, v8, v9
	ds_read2_b32 v[8:9], v6 offset0:132 offset1:165
	s_waitcnt lgkmcnt(4)
	v_med3_f32 v53, v56, s24, v49
	v_med3_f32 v55, v57, s24, v49
	v_cvt_pk_fp8_f32 v54, v53, v55 op_sel:[0,0,1]
	ds_read2_b32 v[56:57], v6 offset0:198 offset1:231
	s_waitcnt lgkmcnt(1)
	v_med3_f32 v8, v8, s24, v49
	v_med3_f32 v9, v9, s24, v49
	v_mov_b32_e32 v55, v3
	v_cvt_pk_fp8_f32 v55, v8, v9
	ds_read2_b32 v[8:9], v50 offset0:8 offset1:41
	s_waitcnt lgkmcnt(1)
	v_med3_f32 v53, v56, s24, v49
	v_med3_f32 v56, v57, s24, v49
	v_cvt_pk_fp8_f32 v55, v53, v56 op_sel:[0,0,1]
	v_mov_b32_e32 v56, v3
	s_waitcnt lgkmcnt(0)
	v_med3_f32 v8, v8, s24, v49
	v_med3_f32 v9, v9, s24, v49
	v_cvt_pk_fp8_f32 v56, v8, v9
	ds_read2_b32 v[8:9], v50 offset0:140 offset1:173
	v_med3_f32 v53, v58, s24, v49
	v_med3_f32 v57, v59, s24, v49
	v_cvt_pk_fp8_f32 v56, v53, v57 op_sel:[0,0,1]
	ds_read2_b32 v[58:59], v50 offset0:206 offset1:239
	s_waitcnt lgkmcnt(1)
	v_med3_f32 v8, v8, s24, v49
	v_med3_f32 v9, v9, s24, v49
	v_mov_b32_e32 v57, v3
	v_cvt_pk_fp8_f32 v57, v8, v9
	ds_read2_b32 v[8:9], v51 offset0:16 offset1:49
	s_waitcnt lgkmcnt(1)
	v_med3_f32 v53, v58, s24, v49
	v_med3_f32 v58, v59, s24, v49
	v_cvt_pk_fp8_f32 v57, v53, v58 op_sel:[0,0,1]
	v_mov_b32_e32 v58, v3
	s_waitcnt lgkmcnt(0)
	v_med3_f32 v8, v8, s24, v49
	v_med3_f32 v9, v9, s24, v49
	v_cvt_pk_fp8_f32 v58, v8, v9
	ds_read2_b32 v[8:9], v51 offset0:148 offset1:181
	v_med3_f32 v53, v60, s24, v49
	v_med3_f32 v59, v61, s24, v49
	v_cvt_pk_fp8_f32 v58, v53, v59 op_sel:[0,0,1]
	ds_read2_b32 v[60:61], v51 offset0:214 offset1:247
	s_waitcnt lgkmcnt(1)
	v_med3_f32 v8, v8, s24, v49
	v_med3_f32 v9, v9, s24, v49
	v_mov_b32_e32 v59, v3
	v_cvt_pk_fp8_f32 v59, v8, v9
	ds_read2_b32 v[8:9], v52 offset0:24 offset1:57
	s_waitcnt lgkmcnt(1)
	v_med3_f32 v53, v60, s24, v49
	v_med3_f32 v60, v61, s24, v49
	v_cvt_pk_fp8_f32 v59, v53, v60 op_sel:[0,0,1]
	v_med3_f32 v64, v62, s24, v49
	s_waitcnt lgkmcnt(0)
	v_med3_f32 v53, v8, s24, v49
	v_med3_f32 v61, v9, s24, v49
	ds_read2_b32 v[8:9], v52 offset0:156 offset1:189
	v_med3_f32 v65, v63, s24, v49
	v_mov_b32_e32 v60, v3
	ds_read2_b32 v[62:63], v52 offset0:222 offset1:255
	v_cvt_pk_fp8_f32 v60, v53, v61
	s_waitcnt lgkmcnt(1)
	v_med3_f32 v8, v8, s24, v49
	v_med3_f32 v9, v9, s24, v49
	v_mov_b32_e32 v61, v3
	v_cvt_pk_fp8_f32 v61, v8, v9
	s_waitcnt lgkmcnt(0)
	v_med3_f32 v8, v62, s24, v49
	v_med3_f32 v9, v63, s24, v49
	v_cvt_pk_fp8_f32 v60, v64, v65 op_sel:[0,0,1]
	v_cvt_pk_fp8_f32 v61, v8, v9 op_sel:[0,0,1]
	v_or_b32_e32 v8, s6, v0
	v_ashrrev_i32_e32 v9, 31, v8
	v_lshlrev_b64 v[8:9], 10, v[8:9]
	v_lshl_add_u64 v[8:9], s[2:3], 0, v[8:9]
	v_lshl_add_u64 v[8:9], v[8:9], 0, s[4:5]
	v_lshl_add_u64 v[8:9], v[8:9], 0, v[4:5]
	global_store_dwordx4 v[8:9], v[54:57], off
	global_store_dwordx4 v[8:9], v[58:61], off offset:16
	s_waitcnt lgkmcnt(0)
	s_branch .LBB0_1480
